# attention epilogue: shfl_xor(1) via DPP quad_perm instead of ds_bpermute (on top of MoE changes)
# speedup vs baseline: 1.0718x; 1.0057x over previous
.LBB0_1497:
	s_and_saveexec_b64 s[20:21], s[2:3]
	ds_write_b32 v184, v204
	s_or_b64 exec, exec, s[20:21]
	s_lshl_b64 s[2:3], s[16:17], 23
	s_add_u32 s2, s28, s2
	s_addc_u32 s3, s29, s3
	s_lshl_b32 s16, s19, 8
	s_add_u32 s20, s2, s16
	s_addc_u32 s21, s3, 0
	s_ashr_i32 s19, s18, 31
	v_and_b32_e32 v66, 64, v215
	s_lshl_b64 s[2:3], s[18:19], 12
	v_lshlrev_b32_e32 v70, 14, v1
	v_xor_b32_e32 v1, 1, v215
	v_add_u32_e32 v66, 64, v66
	s_waitcnt lgkmcnt(0)
	s_add_u32 s16, s20, s2
	v_cmp_lt_i32_e32 vcc, v1, v66
	v_and_b32_e32 v66, 1, v178
	v_add_u32_e32 v72, s42, v168
	s_addc_u32 s17, s21, s3
	v_cmp_eq_u32_e64 s[2:3], 0, v66
	ds_read_b128 v[66:69], v72
	v_cndmask_b32_e32 v1, v215, v1, vcc
	v_lshlrev_b32_e32 v1, 2, v1
	v_lshlrev_b32_e32 v86, 1, v179
	v_lshl_add_u64 v[74:75], s[16:17], 0, v[86:87]
	s_waitcnt lgkmcnt(0)
	v_rcp_f32_e32 v66, v66
	v_mov_b32_e32 v71, v87
	v_lshl_add_u64 v[70:71], v[74:75], 0, v[70:71]
	v_mul_f32_e32 v50, v50, v66
	s_nop 1
	v_mov_b32_dpp v73, v50 quad_perm:[1,0,3,2] row_mask:0xf bank_mask:0xf
	s_and_saveexec_b64 s[16:17], s[2:3]
	s_cbranch_execz .LBB0_1501
	s_waitcnt lgkmcnt(0)
	v_cvt_pk_bf16_f32 v50, v50, v73
	global_store_dword v[70:71], v50, off
.LBB0_1501:
	s_or_b64 exec, exec, s[16:17]
	v_mul_f32_e32 v34, v34, v66
	s_nop 1
	v_mov_b32_dpp v50, v34 quad_perm:[1,0,3,2] row_mask:0xf bank_mask:0xf
	s_and_saveexec_b64 s[16:17], s[2:3]
	s_cbranch_execz .LBB0_1503
	s_waitcnt lgkmcnt(0)
	v_cvt_pk_bf16_f32 v34, v34, v50
	global_store_dword v[70:71], v34, off offset:64
.LBB0_1503:
	s_or_b64 exec, exec, s[16:17]
	v_mul_f32_e32 v18, v18, v66
	s_nop 1
	v_mov_b32_dpp v34, v18 quad_perm:[1,0,3,2] row_mask:0xf bank_mask:0xf
	s_and_saveexec_b64 s[16:17], s[2:3]
	s_cbranch_execz .LBB0_1505
	s_waitcnt lgkmcnt(0)
	v_cvt_pk_bf16_f32 v18, v18, v34
	global_store_dword v[70:71], v18, off offset:128
.LBB0_1505:
	s_or_b64 exec, exec, s[16:17]
	v_mul_f32_e32 v2, v2, v66
	s_nop 1
	v_mov_b32_dpp v18, v2 quad_perm:[1,0,3,2] row_mask:0xf bank_mask:0xf
	s_and_saveexec_b64 s[16:17], s[2:3]
	s_cbranch_execz .LBB0_1507
	s_waitcnt lgkmcnt(0)
	v_cvt_pk_bf16_f32 v2, v2, v18
	global_store_dword v[70:71], v2, off offset:192
.LBB0_1507:
	s_or_b64 exec, exec, s[16:17]
	v_rcp_f32_e32 v2, v67
	s_waitcnt lgkmcnt(0)
	v_mul_f32_e32 v18, v51, v2
	s_nop 1
	v_mov_b32_dpp v34, v18 quad_perm:[1,0,3,2] row_mask:0xf bank_mask:0xf
	s_and_saveexec_b64 s[16:17], s[2:3]
	s_cbranch_execz .LBB0_1509
	v_add_co_u32_e32 v50, vcc, 0x1000, v70
	s_waitcnt lgkmcnt(0)
	v_cvt_pk_bf16_f32 v18, v18, v34
	s_nop 0
	v_addc_co_u32_e32 v51, vcc, 0, v71, vcc
	global_store_dword v[50:51], v18, off
.LBB0_1509:
	s_or_b64 exec, exec, s[16:17]
	v_mul_f32_e32 v18, v35, v2
	s_waitcnt lgkmcnt(0)
	s_nop 1
	v_mov_b32_dpp v34, v18 quad_perm:[1,0,3,2] row_mask:0xf bank_mask:0xf
	s_and_saveexec_b64 s[16:17], s[2:3]
	s_cbranch_execz .LBB0_1511
	s_waitcnt lgkmcnt(0)
	v_cvt_pk_bf16_f32 v18, v18, v34
	v_add_co_u32_e32 v34, vcc, 0x1000, v70
	s_nop 1
	v_addc_co_u32_e32 v35, vcc, 0, v71, vcc
	global_store_dword v[34:35], v18, off offset:64
.LBB0_1511:
	s_or_b64 exec, exec, s[16:17]
	v_mul_f32_e32 v18, v19, v2
	s_nop 1
	v_mov_b32_dpp v19, v18 quad_perm:[1,0,3,2] row_mask:0xf bank_mask:0xf
	s_and_saveexec_b64 s[16:17], s[2:3]
	s_cbranch_execz .LBB0_1513
	s_waitcnt lgkmcnt(0)
	v_cvt_pk_bf16_f32 v34, v18, v19
	v_add_co_u32_e32 v18, vcc, 0x1000, v70
	s_nop 1
	v_addc_co_u32_e32 v19, vcc, 0, v71, vcc
	global_store_dword v[18:19], v34, off offset:128
.LBB0_1513:
	s_or_b64 exec, exec, s[16:17]
	v_mul_f32_e32 v2, v3, v2
	s_nop 1
	v_mov_b32_dpp v3, v2 quad_perm:[1,0,3,2] row_mask:0xf bank_mask:0xf
	s_and_saveexec_b64 s[16:17], s[2:3]
	s_cbranch_execz .LBB0_1515
	s_waitcnt lgkmcnt(0)
	v_cvt_pk_bf16_f32 v18, v2, v3
	v_add_co_u32_e32 v2, vcc, 0x1000, v70
	s_nop 1
	v_addc_co_u32_e32 v3, vcc, 0, v71, vcc
	global_store_dword v[2:3], v18, off offset:192
.LBB0_1515:
	s_or_b64 exec, exec, s[16:17]
	v_rcp_f32_e32 v2, v68
	s_waitcnt lgkmcnt(0)
	v_mul_f32_e32 v3, v52, v2
	s_nop 1
	v_mov_b32_dpp v18, v3 quad_perm:[1,0,3,2] row_mask:0xf bank_mask:0xf
	s_and_saveexec_b64 s[16:17], s[2:3]
	s_cbranch_execz .LBB0_1517
	s_waitcnt lgkmcnt(0)
	v_cvt_pk_bf16_f32 v3, v3, v18
	v_add_co_u32_e32 v18, vcc, 0x2000, v70
	s_nop 1
	v_addc_co_u32_e32 v19, vcc, 0, v71, vcc
	global_store_dword v[18:19], v3, off
.LBB0_1517:
	s_or_b64 exec, exec, s[16:17]
	v_mul_f32_e32 v3, v36, v2
	s_waitcnt lgkmcnt(0)
	s_nop 1
	v_mov_b32_dpp v18, v3 quad_perm:[1,0,3,2] row_mask:0xf bank_mask:0xf
	s_and_saveexec_b64 s[16:17], s[2:3]
	s_cbranch_execz .LBB0_1519
	s_waitcnt lgkmcnt(0)
	v_cvt_pk_bf16_f32 v3, v3, v18
	v_add_co_u32_e32 v18, vcc, 0x2000, v70
	s_nop 1
	v_addc_co_u32_e32 v19, vcc, 0, v71, vcc
	global_store_dword v[18:19], v3, off offset:64
.LBB0_1519:
	s_or_b64 exec, exec, s[16:17]
	v_mul_f32_e32 v3, v20, v2
	s_waitcnt lgkmcnt(0)
	s_nop 1
	v_mov_b32_dpp v18, v3 quad_perm:[1,0,3,2] row_mask:0xf bank_mask:0xf
	s_and_saveexec_b64 s[16:17], s[2:3]
	s_cbranch_execz .LBB0_1521
	s_waitcnt lgkmcnt(0)
	v_cvt_pk_bf16_f32 v3, v3, v18
	v_add_co_u32_e32 v18, vcc, 0x2000, v70
	s_nop 1
	v_addc_co_u32_e32 v19, vcc, 0, v71, vcc
	global_store_dword v[18:19], v3, off offset:128
.LBB0_1521:
	s_or_b64 exec, exec, s[16:17]
	v_mul_f32_e32 v2, v4, v2
	s_nop 1
	v_mov_b32_dpp v3, v2 quad_perm:[1,0,3,2] row_mask:0xf bank_mask:0xf
	s_and_saveexec_b64 s[16:17], s[2:3]
	s_cbranch_execz .LBB0_1523
	s_waitcnt lgkmcnt(0)
	v_cvt_pk_bf16_f32 v4, v2, v3
	v_add_co_u32_e32 v2, vcc, 0x2000, v70
	s_nop 1
	v_addc_co_u32_e32 v3, vcc, 0, v71, vcc
	global_store_dword v[2:3], v4, off offset:192
.LBB0_1523:
	s_or_b64 exec, exec, s[16:17]
	v_rcp_f32_e32 v2, v69
	s_waitcnt lgkmcnt(0)
	v_mul_f32_e32 v3, v53, v2
	s_nop 1
	v_mov_b32_dpp v4, v3 quad_perm:[1,0,3,2] row_mask:0xf bank_mask:0xf
	s_and_saveexec_b64 s[16:17], s[2:3]
	s_cbranch_execz .LBB0_1525
	v_add_co_u32_e32 v18, vcc, 0x3000, v70
	s_waitcnt lgkmcnt(0)
	v_cvt_pk_bf16_f32 v3, v3, v4
	s_nop 0
	v_addc_co_u32_e32 v19, vcc, 0, v71, vcc
	global_store_dword v[18:19], v3, off
.LBB0_1525:
	s_or_b64 exec, exec, s[16:17]
	v_mul_f32_e32 v3, v37, v2
	s_waitcnt lgkmcnt(0)
	s_nop 1
	v_mov_b32_dpp v4, v3 quad_perm:[1,0,3,2] row_mask:0xf bank_mask:0xf
	s_and_saveexec_b64 s[16:17], s[2:3]
	s_cbranch_execz .LBB0_1527
	v_add_co_u32_e32 v18, vcc, 0x3000, v70
	s_waitcnt lgkmcnt(0)
	v_cvt_pk_bf16_f32 v3, v3, v4
	s_nop 0
	v_addc_co_u32_e32 v19, vcc, 0, v71, vcc
	global_store_dword v[18:19], v3, off offset:64
.LBB0_1527:
	s_or_b64 exec, exec, s[16:17]
	v_mul_f32_e32 v3, v21, v2
	s_waitcnt lgkmcnt(0)
	s_nop 1
	v_mov_b32_dpp v4, v3 quad_perm:[1,0,3,2] row_mask:0xf bank_mask:0xf
	s_and_saveexec_b64 s[16:17], s[2:3]
	s_cbranch_execz .LBB0_1529
	v_add_co_u32_e32 v18, vcc, 0x3000, v70
	s_waitcnt lgkmcnt(0)
	v_cvt_pk_bf16_f32 v3, v3, v4
	s_nop 0
	v_addc_co_u32_e32 v19, vcc, 0, v71, vcc
	global_store_dword v[18:19], v3, off offset:128
.LBB0_1529:
	s_or_b64 exec, exec, s[16:17]
	v_mul_f32_e32 v2, v5, v2
	s_nop 1
	v_mov_b32_dpp v3, v2 quad_perm:[1,0,3,2] row_mask:0xf bank_mask:0xf
	s_and_saveexec_b64 s[16:17], s[2:3]
	s_cbranch_execz .LBB0_1531
	s_waitcnt lgkmcnt(0)
	v_cvt_pk_bf16_f32 v4, v2, v3
	v_add_co_u32_e32 v2, vcc, 0x3000, v70
	s_nop 1
	v_addc_co_u32_e32 v3, vcc, 0, v71, vcc
	global_store_dword v[2:3], v4, off offset:192
.LBB0_1531:
	s_or_b64 exec, exec, s[16:17]
	s_waitcnt lgkmcnt(0)
	ds_read_b128 v[2:5], v72 offset:32
	s_waitcnt lgkmcnt(0)
	v_rcp_f32_e32 v2, v2
	s_nop 0
	v_mul_f32_e32 v18, v54, v2
	s_nop 1
	v_mov_b32_dpp v19, v18 quad_perm:[1,0,3,2] row_mask:0xf bank_mask:0xf
	s_and_saveexec_b64 s[16:17], s[2:3]
	s_cbranch_execz .LBB0_1533
	s_waitcnt lgkmcnt(0)
	v_cvt_pk_bf16_f32 v20, v18, v19
	v_add_co_u32_e32 v18, vcc, 0x8000, v70
	s_nop 1
	v_addc_co_u32_e32 v19, vcc, 0, v71, vcc
	global_store_dword v[18:19], v20, off
.LBB0_1533:
	s_or_b64 exec, exec, s[16:17]
	v_mul_f32_e32 v18, v38, v2
	s_waitcnt lgkmcnt(0)
	s_nop 1
	v_mov_b32_dpp v19, v18 quad_perm:[1,0,3,2] row_mask:0xf bank_mask:0xf
	s_and_saveexec_b64 s[16:17], s[2:3]
	s_cbranch_execz .LBB0_1535
	s_waitcnt lgkmcnt(0)
	v_cvt_pk_bf16_f32 v20, v18, v19
	v_add_co_u32_e32 v18, vcc, 0x8000, v70
	s_nop 1
	v_addc_co_u32_e32 v19, vcc, 0, v71, vcc
	global_store_dword v[18:19], v20, off offset:64
.LBB0_1535:
	s_or_b64 exec, exec, s[16:17]
	v_mul_f32_e32 v18, v22, v2
	s_waitcnt lgkmcnt(0)
	s_nop 1
	v_mov_b32_dpp v19, v18 quad_perm:[1,0,3,2] row_mask:0xf bank_mask:0xf
	s_and_saveexec_b64 s[16:17], s[2:3]
	s_cbranch_execz .LBB0_1537
	s_waitcnt lgkmcnt(0)
	v_cvt_pk_bf16_f32 v20, v18, v19
	v_add_co_u32_e32 v18, vcc, 0x8000, v70
	s_nop 1
	v_addc_co_u32_e32 v19, vcc, 0, v71, vcc
	global_store_dword v[18:19], v20, off offset:128
.LBB0_1537:
	s_or_b64 exec, exec, s[16:17]
	v_mul_f32_e32 v2, v6, v2
	s_nop 1
	v_mov_b32_dpp v6, v2 quad_perm:[1,0,3,2] row_mask:0xf bank_mask:0xf
	s_and_saveexec_b64 s[16:17], s[2:3]
	s_cbranch_execz .LBB0_1539
	v_add_co_u32_e32 v18, vcc, 0x8000, v70
	s_waitcnt lgkmcnt(0)
	v_cvt_pk_bf16_f32 v2, v2, v6
	s_nop 0
	v_addc_co_u32_e32 v19, vcc, 0, v71, vcc
	global_store_dword v[18:19], v2, off offset:192
.LBB0_1539:
	s_or_b64 exec, exec, s[16:17]
	v_rcp_f32_e32 v2, v3
	s_nop 0
	v_mul_f32_e32 v3, v55, v2
	s_waitcnt lgkmcnt(0)
	s_nop 1
	v_mov_b32_dpp v6, v3 quad_perm:[1,0,3,2] row_mask:0xf bank_mask:0xf
	s_and_saveexec_b64 s[16:17], s[2:3]
	s_cbranch_execz .LBB0_1541
	v_add_co_u32_e32 v18, vcc, 0x9000, v70
	s_waitcnt lgkmcnt(0)
	v_cvt_pk_bf16_f32 v3, v3, v6
	s_nop 0
	v_addc_co_u32_e32 v19, vcc, 0, v71, vcc
	global_store_dword v[18:19], v3, off
.LBB0_1541:
	s_or_b64 exec, exec, s[16:17]
	v_mul_f32_e32 v3, v39, v2
	s_waitcnt lgkmcnt(0)
	s_nop 1
	v_mov_b32_dpp v6, v3 quad_perm:[1,0,3,2] row_mask:0xf bank_mask:0xf
	s_and_saveexec_b64 s[16:17], s[2:3]
	s_cbranch_execz .LBB0_1543
	v_add_co_u32_e32 v18, vcc, 0x9000, v70
	s_waitcnt lgkmcnt(0)
	v_cvt_pk_bf16_f32 v3, v3, v6
	s_nop 0
	v_addc_co_u32_e32 v19, vcc, 0, v71, vcc
	global_store_dword v[18:19], v3, off offset:64
.LBB0_1543:
	s_or_b64 exec, exec, s[16:17]
	v_mul_f32_e32 v3, v23, v2
	s_waitcnt lgkmcnt(0)
	s_nop 1
	v_mov_b32_dpp v6, v3 quad_perm:[1,0,3,2] row_mask:0xf bank_mask:0xf
	s_and_saveexec_b64 s[16:17], s[2:3]
	s_cbranch_execz .LBB0_1545
	v_add_co_u32_e32 v18, vcc, 0x9000, v70
	s_waitcnt lgkmcnt(0)
	v_cvt_pk_bf16_f32 v3, v3, v6
	s_nop 0
	v_addc_co_u32_e32 v19, vcc, 0, v71, vcc
	global_store_dword v[18:19], v3, off offset:128
.LBB0_1545:
	s_or_b64 exec, exec, s[16:17]
	v_mul_f32_e32 v2, v7, v2
	s_nop 1
	v_mov_b32_dpp v3, v2 quad_perm:[1,0,3,2] row_mask:0xf bank_mask:0xf
	s_and_saveexec_b64 s[16:17], s[2:3]
	s_cbranch_execz .LBB0_1547
	s_waitcnt lgkmcnt(0)
	v_cvt_pk_bf16_f32 v6, v2, v3
	v_add_co_u32_e32 v2, vcc, 0x9000, v70
	s_nop 1
	v_addc_co_u32_e32 v3, vcc, 0, v71, vcc
	global_store_dword v[2:3], v6, off offset:192
.LBB0_1547:
	s_or_b64 exec, exec, s[16:17]
	v_rcp_f32_e32 v2, v4
	s_waitcnt lgkmcnt(0)
	v_mul_f32_e32 v3, v56, v2
	s_nop 1
	v_mov_b32_dpp v4, v3 quad_perm:[1,0,3,2] row_mask:0xf bank_mask:0xf
	s_and_saveexec_b64 s[16:17], s[2:3]
	s_cbranch_execz .LBB0_1549
	v_add_co_u32_e32 v6, vcc, 0xa000, v70
	s_waitcnt lgkmcnt(0)
	v_cvt_pk_bf16_f32 v3, v3, v4
	s_nop 0
	v_addc_co_u32_e32 v7, vcc, 0, v71, vcc
	global_store_dword v[6:7], v3, off
.LBB0_1549:
	s_or_b64 exec, exec, s[16:17]
	v_mul_f32_e32 v3, v40, v2
	s_waitcnt lgkmcnt(0)
	s_nop 1
	v_mov_b32_dpp v4, v3 quad_perm:[1,0,3,2] row_mask:0xf bank_mask:0xf
	s_and_saveexec_b64 s[16:17], s[2:3]
	s_cbranch_execz .LBB0_1551
	v_add_co_u32_e32 v6, vcc, 0xa000, v70
	s_waitcnt lgkmcnt(0)
	v_cvt_pk_bf16_f32 v3, v3, v4
	s_nop 0
	v_addc_co_u32_e32 v7, vcc, 0, v71, vcc
	global_store_dword v[6:7], v3, off offset:64
.LBB0_1551:
	s_or_b64 exec, exec, s[16:17]
	v_mul_f32_e32 v3, v24, v2
	s_waitcnt lgkmcnt(0)
	s_nop 1
	v_mov_b32_dpp v4, v3 quad_perm:[1,0,3,2] row_mask:0xf bank_mask:0xf
	s_and_saveexec_b64 s[16:17], s[2:3]
	s_cbranch_execz .LBB0_1553
	v_add_co_u32_e32 v6, vcc, 0xa000, v70
	s_waitcnt lgkmcnt(0)
	v_cvt_pk_bf16_f32 v3, v3, v4
	s_nop 0
	v_addc_co_u32_e32 v7, vcc, 0, v71, vcc
	global_store_dword v[6:7], v3, off offset:128
.LBB0_1553:
	s_or_b64 exec, exec, s[16:17]
	v_mul_f32_e32 v2, v8, v2
	s_nop 1
	v_mov_b32_dpp v3, v2 quad_perm:[1,0,3,2] row_mask:0xf bank_mask:0xf
	s_and_saveexec_b64 s[16:17], s[2:3]
	s_cbranch_execz .LBB0_1555
	s_waitcnt lgkmcnt(0)
	v_cvt_pk_bf16_f32 v4, v2, v3
	v_add_co_u32_e32 v2, vcc, 0xa000, v70
	s_nop 1
	v_addc_co_u32_e32 v3, vcc, 0, v71, vcc
	global_store_dword v[2:3], v4, off offset:192
.LBB0_1555:
	s_or_b64 exec, exec, s[16:17]
	v_rcp_f32_e32 v2, v5
	s_waitcnt lgkmcnt(0)
	v_mul_f32_e32 v3, v57, v2
	s_nop 1
	v_mov_b32_dpp v4, v3 quad_perm:[1,0,3,2] row_mask:0xf bank_mask:0xf
	s_and_saveexec_b64 s[16:17], s[2:3]
	s_cbranch_execz .LBB0_1557
	s_waitcnt lgkmcnt(0)
	v_cvt_pk_bf16_f32 v3, v3, v4
	v_add_co_u32_e32 v4, vcc, 0xb000, v70
	s_nop 1
	v_addc_co_u32_e32 v5, vcc, 0, v71, vcc
	global_store_dword v[4:5], v3, off
.LBB0_1557:
	s_or_b64 exec, exec, s[16:17]
	v_mul_f32_e32 v3, v41, v2
	s_waitcnt lgkmcnt(0)
	s_nop 1
	v_mov_b32_dpp v4, v3 quad_perm:[1,0,3,2] row_mask:0xf bank_mask:0xf
	s_and_saveexec_b64 s[16:17], s[2:3]
	s_cbranch_execz .LBB0_1559
	s_waitcnt lgkmcnt(0)
	v_cvt_pk_bf16_f32 v3, v3, v4
	v_add_co_u32_e32 v4, vcc, 0xb000, v70
	s_nop 1
	v_addc_co_u32_e32 v5, vcc, 0, v71, vcc
	global_store_dword v[4:5], v3, off offset:64
.LBB0_1559:
	s_or_b64 exec, exec, s[16:17]
	v_mul_f32_e32 v3, v25, v2
	s_waitcnt lgkmcnt(0)
	s_nop 1
	v_mov_b32_dpp v4, v3 quad_perm:[1,0,3,2] row_mask:0xf bank_mask:0xf
	s_and_saveexec_b64 s[16:17], s[2:3]
	s_cbranch_execz .LBB0_1561
	s_waitcnt lgkmcnt(0)
	v_cvt_pk_bf16_f32 v3, v3, v4
	v_add_co_u32_e32 v4, vcc, 0xb000, v70
	s_nop 1
	v_addc_co_u32_e32 v5, vcc, 0, v71, vcc
	global_store_dword v[4:5], v3, off offset:128
.LBB0_1561:
	s_or_b64 exec, exec, s[16:17]
	v_mul_f32_e32 v2, v9, v2
	s_nop 1
	v_mov_b32_dpp v3, v2 quad_perm:[1,0,3,2] row_mask:0xf bank_mask:0xf
	s_and_saveexec_b64 s[16:17], s[2:3]
	s_cbranch_execz .LBB0_1563
	s_waitcnt lgkmcnt(0)
	v_cvt_pk_bf16_f32 v4, v2, v3
	v_add_co_u32_e32 v2, vcc, 0xb000, v70
	s_nop 1
	v_addc_co_u32_e32 v3, vcc, 0, v71, vcc
	global_store_dword v[2:3], v4, off offset:192
.LBB0_1563:
	s_or_b64 exec, exec, s[16:17]
	s_waitcnt lgkmcnt(0)
	ds_read_b128 v[2:5], v72 offset:64
	s_waitcnt lgkmcnt(0)
	v_rcp_f32_e32 v2, v2
	s_nop 0
	v_mul_f32_e32 v6, v58, v2
	s_nop 1
	v_mov_b32_dpp v7, v6 quad_perm:[1,0,3,2] row_mask:0xf bank_mask:0xf
	s_and_saveexec_b64 s[16:17], s[2:3]
	s_cbranch_execz .LBB0_1565
	s_waitcnt lgkmcnt(0)
	v_cvt_pk_bf16_f32 v8, v6, v7
	v_add_co_u32_e32 v6, vcc, 0x10000, v70
	s_nop 1
	v_addc_co_u32_e32 v7, vcc, 0, v71, vcc
	global_store_dword v[6:7], v8, off
.LBB0_1565:
	s_or_b64 exec, exec, s[16:17]
	v_mul_f32_e32 v6, v42, v2
	s_waitcnt lgkmcnt(0)
	s_nop 1
	v_mov_b32_dpp v7, v6 quad_perm:[1,0,3,2] row_mask:0xf bank_mask:0xf
	s_and_saveexec_b64 s[16:17], s[2:3]
	s_cbranch_execz .LBB0_1567
	s_waitcnt lgkmcnt(0)
	v_cvt_pk_bf16_f32 v8, v6, v7
	v_add_co_u32_e32 v6, vcc, 0x10000, v70
	s_nop 1
	v_addc_co_u32_e32 v7, vcc, 0, v71, vcc
	global_store_dword v[6:7], v8, off offset:64
.LBB0_1567:
	s_or_b64 exec, exec, s[16:17]
	v_mul_f32_e32 v6, v26, v2
	s_waitcnt lgkmcnt(0)
	s_nop 1
	v_mov_b32_dpp v7, v6 quad_perm:[1,0,3,2] row_mask:0xf bank_mask:0xf
	s_and_saveexec_b64 s[16:17], s[2:3]
	s_cbranch_execz .LBB0_1569
	s_waitcnt lgkmcnt(0)
	v_cvt_pk_bf16_f32 v8, v6, v7
	v_add_co_u32_e32 v6, vcc, 0x10000, v70
	s_nop 1
	v_addc_co_u32_e32 v7, vcc, 0, v71, vcc
	global_store_dword v[6:7], v8, off offset:128
.LBB0_1569:
	s_or_b64 exec, exec, s[16:17]
	v_mul_f32_e32 v2, v10, v2
	s_nop 1
	v_mov_b32_dpp v6, v2 quad_perm:[1,0,3,2] row_mask:0xf bank_mask:0xf
	s_and_saveexec_b64 s[16:17], s[2:3]
	s_cbranch_execz .LBB0_1571
	s_waitcnt lgkmcnt(0)
	v_cvt_pk_bf16_f32 v2, v2, v6
	v_add_co_u32_e32 v6, vcc, 0x10000, v70
	s_nop 1
	v_addc_co_u32_e32 v7, vcc, 0, v71, vcc
	global_store_dword v[6:7], v2, off offset:192
.LBB0_1571:
	s_or_b64 exec, exec, s[16:17]
	v_rcp_f32_e32 v2, v3
	s_nop 0
	v_mul_f32_e32 v3, v59, v2
	s_waitcnt lgkmcnt(0)
	s_nop 1
	v_mov_b32_dpp v6, v3 quad_perm:[1,0,3,2] row_mask:0xf bank_mask:0xf
	s_and_saveexec_b64 s[16:17], s[2:3]
	s_cbranch_execz .LBB0_1573
	s_waitcnt lgkmcnt(0)
	v_cvt_pk_bf16_f32 v3, v3, v6
	v_add_co_u32_e32 v6, vcc, 0x11000, v70
	s_nop 1
	v_addc_co_u32_e32 v7, vcc, 0, v71, vcc
	global_store_dword v[6:7], v3, off
.LBB0_1573:
	s_or_b64 exec, exec, s[16:17]
	v_mul_f32_e32 v3, v43, v2
	s_waitcnt lgkmcnt(0)
	s_nop 1
	v_mov_b32_dpp v6, v3 quad_perm:[1,0,3,2] row_mask:0xf bank_mask:0xf
	s_and_saveexec_b64 s[16:17], s[2:3]
	s_cbranch_execz .LBB0_1575
	s_waitcnt lgkmcnt(0)
	v_cvt_pk_bf16_f32 v3, v3, v6
	v_add_co_u32_e32 v6, vcc, 0x11000, v70
	s_nop 1
	v_addc_co_u32_e32 v7, vcc, 0, v71, vcc
	global_store_dword v[6:7], v3, off offset:64
.LBB0_1575:
	s_or_b64 exec, exec, s[16:17]
	v_mul_f32_e32 v3, v27, v2
	s_waitcnt lgkmcnt(0)
	s_nop 1
	v_mov_b32_dpp v6, v3 quad_perm:[1,0,3,2] row_mask:0xf bank_mask:0xf
	s_and_saveexec_b64 s[16:17], s[2:3]
	s_cbranch_execz .LBB0_1577
	s_waitcnt lgkmcnt(0)
	v_cvt_pk_bf16_f32 v3, v3, v6
	v_add_co_u32_e32 v6, vcc, 0x11000, v70
	s_nop 1
	v_addc_co_u32_e32 v7, vcc, 0, v71, vcc
	global_store_dword v[6:7], v3, off offset:128
.LBB0_1577:
	s_or_b64 exec, exec, s[16:17]
	v_mul_f32_e32 v2, v11, v2
	s_nop 1
	v_mov_b32_dpp v3, v2 quad_perm:[1,0,3,2] row_mask:0xf bank_mask:0xf
	s_and_saveexec_b64 s[16:17], s[2:3]
	s_cbranch_execz .LBB0_1579
	s_waitcnt lgkmcnt(0)
	v_cvt_pk_bf16_f32 v6, v2, v3
	v_add_co_u32_e32 v2, vcc, 0x11000, v70
	s_nop 1
	v_addc_co_u32_e32 v3, vcc, 0, v71, vcc
	global_store_dword v[2:3], v6, off offset:192
.LBB0_1579:
	s_or_b64 exec, exec, s[16:17]
	v_rcp_f32_e32 v2, v4
	s_waitcnt lgkmcnt(0)
	v_mul_f32_e32 v3, v60, v2
	s_nop 1
	v_mov_b32_dpp v4, v3 quad_perm:[1,0,3,2] row_mask:0xf bank_mask:0xf
	s_and_saveexec_b64 s[16:17], s[2:3]
	s_cbranch_execz .LBB0_1581
	v_add_co_u32_e32 v6, vcc, 0x12000, v70
	s_waitcnt lgkmcnt(0)
	v_cvt_pk_bf16_f32 v3, v3, v4
	s_nop 0
	v_addc_co_u32_e32 v7, vcc, 0, v71, vcc
	global_store_dword v[6:7], v3, off
.LBB0_1581:
	s_or_b64 exec, exec, s[16:17]
	v_mul_f32_e32 v3, v44, v2
	s_waitcnt lgkmcnt(0)
	s_nop 1
	v_mov_b32_dpp v4, v3 quad_perm:[1,0,3,2] row_mask:0xf bank_mask:0xf
	s_and_saveexec_b64 s[16:17], s[2:3]
	s_cbranch_execz .LBB0_1583
	v_add_co_u32_e32 v6, vcc, 0x12000, v70
	s_waitcnt lgkmcnt(0)
	v_cvt_pk_bf16_f32 v3, v3, v4
	s_nop 0
	v_addc_co_u32_e32 v7, vcc, 0, v71, vcc
	global_store_dword v[6:7], v3, off offset:64
.LBB0_1583:
	s_or_b64 exec, exec, s[16:17]
	v_mul_f32_e32 v3, v28, v2
	s_waitcnt lgkmcnt(0)
	s_nop 1
	v_mov_b32_dpp v4, v3 quad_perm:[1,0,3,2] row_mask:0xf bank_mask:0xf
	s_and_saveexec_b64 s[16:17], s[2:3]
	s_cbranch_execz .LBB0_1585
	v_add_co_u32_e32 v6, vcc, 0x12000, v70
	s_waitcnt lgkmcnt(0)
	v_cvt_pk_bf16_f32 v3, v3, v4
	s_nop 0
	v_addc_co_u32_e32 v7, vcc, 0, v71, vcc
	global_store_dword v[6:7], v3, off offset:128
.LBB0_1585:
	s_or_b64 exec, exec, s[16:17]
	v_mul_f32_e32 v2, v12, v2
	s_nop 1
	v_mov_b32_dpp v3, v2 quad_perm:[1,0,3,2] row_mask:0xf bank_mask:0xf
	s_and_saveexec_b64 s[16:17], s[2:3]
	s_cbranch_execz .LBB0_1587
	s_waitcnt lgkmcnt(0)
	v_cvt_pk_bf16_f32 v4, v2, v3
	v_add_co_u32_e32 v2, vcc, 0x12000, v70
	s_nop 1
	v_addc_co_u32_e32 v3, vcc, 0, v71, vcc
	global_store_dword v[2:3], v4, off offset:192
.LBB0_1587:
	s_or_b64 exec, exec, s[16:17]
	v_rcp_f32_e32 v2, v5
	s_waitcnt lgkmcnt(0)
	v_mul_f32_e32 v3, v61, v2
	s_nop 1
	v_mov_b32_dpp v4, v3 quad_perm:[1,0,3,2] row_mask:0xf bank_mask:0xf
	s_and_saveexec_b64 s[16:17], s[2:3]
	s_cbranch_execz .LBB0_1589
	s_waitcnt lgkmcnt(0)
	v_cvt_pk_bf16_f32 v3, v3, v4
	v_add_co_u32_e32 v4, vcc, 0x13000, v70
	s_nop 1
	v_addc_co_u32_e32 v5, vcc, 0, v71, vcc
	global_store_dword v[4:5], v3, off
.LBB0_1589:
	s_or_b64 exec, exec, s[16:17]
	v_mul_f32_e32 v3, v45, v2
	s_waitcnt lgkmcnt(0)
	s_nop 1
	v_mov_b32_dpp v4, v3 quad_perm:[1,0,3,2] row_mask:0xf bank_mask:0xf
	s_and_saveexec_b64 s[16:17], s[2:3]
	s_cbranch_execz .LBB0_1591
	s_waitcnt lgkmcnt(0)
	v_cvt_pk_bf16_f32 v3, v3, v4
	v_add_co_u32_e32 v4, vcc, 0x13000, v70
	s_nop 1
	v_addc_co_u32_e32 v5, vcc, 0, v71, vcc
	global_store_dword v[4:5], v3, off offset:64
.LBB0_1591:
	s_or_b64 exec, exec, s[16:17]
	v_mul_f32_e32 v3, v29, v2
	s_waitcnt lgkmcnt(0)
	s_nop 1
	v_mov_b32_dpp v4, v3 quad_perm:[1,0,3,2] row_mask:0xf bank_mask:0xf
	s_and_saveexec_b64 s[16:17], s[2:3]
	s_cbranch_execz .LBB0_1593
	s_waitcnt lgkmcnt(0)
	v_cvt_pk_bf16_f32 v3, v3, v4
	v_add_co_u32_e32 v4, vcc, 0x13000, v70
	s_nop 1
	v_addc_co_u32_e32 v5, vcc, 0, v71, vcc
	global_store_dword v[4:5], v3, off offset:128
.LBB0_1593:
	s_or_b64 exec, exec, s[16:17]
	v_mul_f32_e32 v2, v13, v2
	s_nop 1
	v_mov_b32_dpp v3, v2 quad_perm:[1,0,3,2] row_mask:0xf bank_mask:0xf
	s_and_saveexec_b64 s[16:17], s[2:3]
	s_cbranch_execz .LBB0_1595
	s_waitcnt lgkmcnt(0)
	v_cvt_pk_bf16_f32 v4, v2, v3
	v_add_co_u32_e32 v2, vcc, 0x13000, v70
	s_nop 1
	v_addc_co_u32_e32 v3, vcc, 0, v71, vcc
	global_store_dword v[2:3], v4, off offset:192
.LBB0_1595:
	s_or_b64 exec, exec, s[16:17]
	s_waitcnt lgkmcnt(0)
	ds_read_b128 v[2:5], v72 offset:96
	s_waitcnt lgkmcnt(0)
	v_rcp_f32_e32 v2, v2
	s_nop 0
	v_mul_f32_e32 v6, v62, v2
	s_nop 1
	v_mov_b32_dpp v7, v6 quad_perm:[1,0,3,2] row_mask:0xf bank_mask:0xf
	s_and_saveexec_b64 s[16:17], s[2:3]
	s_cbranch_execz .LBB0_1597
	s_waitcnt lgkmcnt(0)
	v_cvt_pk_bf16_f32 v8, v6, v7
	v_add_co_u32_e32 v6, vcc, 0x18000, v70
	s_nop 1
	v_addc_co_u32_e32 v7, vcc, 0, v71, vcc
	global_store_dword v[6:7], v8, off
.LBB0_1597:
	s_or_b64 exec, exec, s[16:17]
	v_mul_f32_e32 v6, v46, v2
	s_waitcnt lgkmcnt(0)
	s_nop 1
	v_mov_b32_dpp v7, v6 quad_perm:[1,0,3,2] row_mask:0xf bank_mask:0xf
	s_and_saveexec_b64 s[16:17], s[2:3]
	s_cbranch_execz .LBB0_1599
	s_waitcnt lgkmcnt(0)
	v_cvt_pk_bf16_f32 v8, v6, v7
	v_add_co_u32_e32 v6, vcc, 0x18000, v70
	s_nop 1
	v_addc_co_u32_e32 v7, vcc, 0, v71, vcc
	global_store_dword v[6:7], v8, off offset:64
.LBB0_1599:
	s_or_b64 exec, exec, s[16:17]
	v_mul_f32_e32 v6, v30, v2
	s_waitcnt lgkmcnt(0)
	s_nop 1
	v_mov_b32_dpp v7, v6 quad_perm:[1,0,3,2] row_mask:0xf bank_mask:0xf
	s_and_saveexec_b64 s[16:17], s[2:3]
	s_cbranch_execz .LBB0_1601
	s_waitcnt lgkmcnt(0)
	v_cvt_pk_bf16_f32 v8, v6, v7
	v_add_co_u32_e32 v6, vcc, 0x18000, v70
	s_nop 1
	v_addc_co_u32_e32 v7, vcc, 0, v71, vcc
	global_store_dword v[6:7], v8, off offset:128
.LBB0_1601:
	s_or_b64 exec, exec, s[16:17]
	v_mul_f32_e32 v2, v14, v2
	s_nop 1
	v_mov_b32_dpp v6, v2 quad_perm:[1,0,3,2] row_mask:0xf bank_mask:0xf
	s_and_saveexec_b64 s[16:17], s[2:3]
	s_cbranch_execz .LBB0_1603
	s_waitcnt lgkmcnt(0)
	v_cvt_pk_bf16_f32 v2, v2, v6
	v_add_co_u32_e32 v6, vcc, 0x18000, v70
	s_nop 1
	v_addc_co_u32_e32 v7, vcc, 0, v71, vcc
	global_store_dword v[6:7], v2, off offset:192
.LBB0_1603:
	s_or_b64 exec, exec, s[16:17]
	v_rcp_f32_e32 v2, v3
	s_nop 0
	v_mul_f32_e32 v3, v63, v2
	s_waitcnt lgkmcnt(0)
	s_nop 1
	v_mov_b32_dpp v6, v3 quad_perm:[1,0,3,2] row_mask:0xf bank_mask:0xf
	s_and_saveexec_b64 s[16:17], s[2:3]
	s_cbranch_execz .LBB0_1605
	s_waitcnt lgkmcnt(0)
	v_cvt_pk_bf16_f32 v3, v3, v6
	v_add_co_u32_e32 v6, vcc, 0x19000, v70
	s_nop 1
	v_addc_co_u32_e32 v7, vcc, 0, v71, vcc
	global_store_dword v[6:7], v3, off
.LBB0_1605:
	s_or_b64 exec, exec, s[16:17]
	v_mul_f32_e32 v3, v47, v2
	s_waitcnt lgkmcnt(0)
	s_nop 1
	v_mov_b32_dpp v6, v3 quad_perm:[1,0,3,2] row_mask:0xf bank_mask:0xf
	s_and_saveexec_b64 s[16:17], s[2:3]
	s_cbranch_execz .LBB0_1607
	s_waitcnt lgkmcnt(0)
	v_cvt_pk_bf16_f32 v3, v3, v6
	v_add_co_u32_e32 v6, vcc, 0x19000, v70
	s_nop 1
	v_addc_co_u32_e32 v7, vcc, 0, v71, vcc
	global_store_dword v[6:7], v3, off offset:64
.LBB0_1607:
	s_or_b64 exec, exec, s[16:17]
	v_mul_f32_e32 v3, v31, v2
	s_waitcnt lgkmcnt(0)
	s_nop 1
	v_mov_b32_dpp v6, v3 quad_perm:[1,0,3,2] row_mask:0xf bank_mask:0xf
	s_and_saveexec_b64 s[16:17], s[2:3]
	s_cbranch_execz .LBB0_1609
	s_waitcnt lgkmcnt(0)
	v_cvt_pk_bf16_f32 v3, v3, v6
	v_add_co_u32_e32 v6, vcc, 0x19000, v70
	s_nop 1
	v_addc_co_u32_e32 v7, vcc, 0, v71, vcc
	global_store_dword v[6:7], v3, off offset:128
.LBB0_1609:
	s_or_b64 exec, exec, s[16:17]
	v_mul_f32_e32 v2, v15, v2
	s_nop 1
	v_mov_b32_dpp v3, v2 quad_perm:[1,0,3,2] row_mask:0xf bank_mask:0xf
	s_and_saveexec_b64 s[16:17], s[2:3]
	s_cbranch_execz .LBB0_1611
	s_waitcnt lgkmcnt(0)
	v_cvt_pk_bf16_f32 v6, v2, v3
	v_add_co_u32_e32 v2, vcc, 0x19000, v70
	s_nop 1
	v_addc_co_u32_e32 v3, vcc, 0, v71, vcc
	global_store_dword v[2:3], v6, off offset:192
.LBB0_1611:
	s_or_b64 exec, exec, s[16:17]
	v_rcp_f32_e32 v2, v4
	s_waitcnt lgkmcnt(0)
	v_mul_f32_e32 v3, v64, v2
	s_nop 1
	v_mov_b32_dpp v4, v3 quad_perm:[1,0,3,2] row_mask:0xf bank_mask:0xf
	s_and_saveexec_b64 s[16:17], s[2:3]
	s_cbranch_execz .LBB0_1613
	v_add_co_u32_e32 v6, vcc, 0x1a000, v70
	s_waitcnt lgkmcnt(0)
	v_cvt_pk_bf16_f32 v3, v3, v4
	s_nop 0
	v_addc_co_u32_e32 v7, vcc, 0, v71, vcc
	global_store_dword v[6:7], v3, off
.LBB0_1613:
	s_or_b64 exec, exec, s[16:17]
	v_mul_f32_e32 v3, v48, v2
	s_waitcnt lgkmcnt(0)
	s_nop 1
	v_mov_b32_dpp v4, v3 quad_perm:[1,0,3,2] row_mask:0xf bank_mask:0xf
	s_and_saveexec_b64 s[16:17], s[2:3]
	s_cbranch_execz .LBB0_1615
	v_add_co_u32_e32 v6, vcc, 0x1a000, v70
	s_waitcnt lgkmcnt(0)
	v_cvt_pk_bf16_f32 v3, v3, v4
	s_nop 0
	v_addc_co_u32_e32 v7, vcc, 0, v71, vcc
	global_store_dword v[6:7], v3, off offset:64
.LBB0_1615:
	s_or_b64 exec, exec, s[16:17]
	v_mul_f32_e32 v3, v32, v2
	s_waitcnt lgkmcnt(0)
	s_nop 1
	v_mov_b32_dpp v4, v3 quad_perm:[1,0,3,2] row_mask:0xf bank_mask:0xf
	s_and_saveexec_b64 s[16:17], s[2:3]
	s_cbranch_execz .LBB0_1617
	v_add_co_u32_e32 v6, vcc, 0x1a000, v70
	s_waitcnt lgkmcnt(0)
	v_cvt_pk_bf16_f32 v3, v3, v4
	s_nop 0
	v_addc_co_u32_e32 v7, vcc, 0, v71, vcc
	global_store_dword v[6:7], v3, off offset:128
.LBB0_1617:
	s_or_b64 exec, exec, s[16:17]
	v_mul_f32_e32 v2, v16, v2
	s_nop 1
	v_mov_b32_dpp v3, v2 quad_perm:[1,0,3,2] row_mask:0xf bank_mask:0xf
	s_and_saveexec_b64 s[16:17], s[2:3]
	s_cbranch_execz .LBB0_1619
	s_waitcnt lgkmcnt(0)
	v_cvt_pk_bf16_f32 v4, v2, v3
	v_add_co_u32_e32 v2, vcc, 0x1a000, v70
	s_nop 1
	v_addc_co_u32_e32 v3, vcc, 0, v71, vcc
	global_store_dword v[2:3], v4, off offset:192
.LBB0_1619:
	s_or_b64 exec, exec, s[16:17]
	v_rcp_f32_e32 v2, v5
	s_waitcnt lgkmcnt(0)
	v_mul_f32_e32 v3, v65, v2
	s_nop 1
	v_mov_b32_dpp v4, v3 quad_perm:[1,0,3,2] row_mask:0xf bank_mask:0xf
	s_and_saveexec_b64 s[16:17], s[2:3]
	s_cbranch_execz .LBB0_1621
	s_waitcnt lgkmcnt(0)
	v_cvt_pk_bf16_f32 v3, v3, v4
	v_add_co_u32_e32 v4, vcc, 0x1b000, v70
	s_nop 1
	v_addc_co_u32_e32 v5, vcc, 0, v71, vcc
	global_store_dword v[4:5], v3, off
.LBB0_1621:
	s_or_b64 exec, exec, s[16:17]
	v_mul_f32_e32 v3, v49, v2
	s_waitcnt lgkmcnt(0)
	s_nop 1
	v_mov_b32_dpp v4, v3 quad_perm:[1,0,3,2] row_mask:0xf bank_mask:0xf
	s_and_saveexec_b64 s[16:17], s[2:3]
	s_cbranch_execz .LBB0_1623
	s_waitcnt lgkmcnt(0)
	v_cvt_pk_bf16_f32 v3, v3, v4
	v_add_co_u32_e32 v4, vcc, 0x1b000, v70
	s_nop 1
	v_addc_co_u32_e32 v5, vcc, 0, v71, vcc
	global_store_dword v[4:5], v3, off offset:64
.LBB0_1623:
	s_or_b64 exec, exec, s[16:17]
	v_mul_f32_e32 v3, v33, v2
	s_waitcnt lgkmcnt(0)
	s_nop 1
	v_mov_b32_dpp v4, v3 quad_perm:[1,0,3,2] row_mask:0xf bank_mask:0xf
	s_and_saveexec_b64 s[16:17], s[2:3]
	s_cbranch_execz .LBB0_1625
	s_waitcnt lgkmcnt(0)
	v_cvt_pk_bf16_f32 v3, v3, v4
	v_add_co_u32_e32 v4, vcc, 0x1b000, v70
	s_nop 1
	v_addc_co_u32_e32 v5, vcc, 0, v71, vcc
	global_store_dword v[4:5], v3, off offset:128
.LBB0_1625:
	s_or_b64 exec, exec, s[16:17]
	v_mul_f32_e32 v2, v17, v2
	s_nop 1
	v_mov_b32_dpp v3, v2 quad_perm:[1,0,3,2] row_mask:0xf bank_mask:0xf
	s_and_saveexec_b64 s[16:17], s[2:3]
	s_cbranch_execz .LBB0_1627
	s_waitcnt lgkmcnt(0)
	v_cvt_pk_bf16_f32 v4, v2, v3
	v_add_co_u32_e32 v2, vcc, 0x1b000, v70
	s_nop 1
	v_addc_co_u32_e32 v3, vcc, 0, v71, vcc
	global_store_dword v[2:3], v4, off offset:192

.LBB0_1649:
	s_and_saveexec_b64 s[0:1], s[2:3]
	ds_write_b32 v185, v205
	s_or_b64 exec, exec, s[0:1]
	s_waitcnt lgkmcnt(0)
	v_add_u32_e32 v72, s11, v168
	ds_read_b128 v[66:69], v72
	s_ashr_i32 s17, s16, 31
	s_lshl_b64 s[0:1], s[16:17], 12
	s_add_u32 s2, s20, s0
	s_addc_u32 s3, s21, s1
	s_waitcnt lgkmcnt(0)
	v_rcp_f32_e32 v66, v66
	v_and_b32_e32 v71, 1, v179
	v_lshlrev_b32_e32 v86, 1, v178
	v_lshlrev_b32_e32 v70, 14, v180
	v_mul_f32_e32 v50, v50, v66
	s_nop 1
	v_mov_b32_dpp v73, v50 quad_perm:[1,0,3,2] row_mask:0xf bank_mask:0xf
	v_cmp_eq_u32_e64 s[0:1], 0, v71
	v_lshl_add_u64 v[74:75], s[2:3], 0, v[86:87]
	v_mov_b32_e32 v71, v87
	v_lshl_add_u64 v[70:71], v[74:75], 0, v[70:71]
	s_and_saveexec_b64 s[2:3], s[0:1]
	s_cbranch_execz .LBB0_1653
	s_waitcnt lgkmcnt(0)
	v_cvt_pk_bf16_f32 v50, v50, v73
	global_store_dword v[70:71], v50, off
.LBB0_1653:
	s_or_b64 exec, exec, s[2:3]
	v_mul_f32_e32 v34, v34, v66
	s_nop 1
	v_mov_b32_dpp v50, v34 quad_perm:[1,0,3,2] row_mask:0xf bank_mask:0xf
	s_and_saveexec_b64 s[2:3], s[0:1]
	s_cbranch_execz .LBB0_1655
	s_waitcnt lgkmcnt(0)
	v_cvt_pk_bf16_f32 v34, v34, v50
	global_store_dword v[70:71], v34, off offset:64
.LBB0_1655:
	s_or_b64 exec, exec, s[2:3]
	v_mul_f32_e32 v18, v18, v66
	s_nop 1
	v_mov_b32_dpp v34, v18 quad_perm:[1,0,3,2] row_mask:0xf bank_mask:0xf
	s_and_saveexec_b64 s[2:3], s[0:1]
	s_cbranch_execz .LBB0_1657
	s_waitcnt lgkmcnt(0)
	v_cvt_pk_bf16_f32 v18, v18, v34
	global_store_dword v[70:71], v18, off offset:128
.LBB0_1657:
	s_or_b64 exec, exec, s[2:3]
	v_mul_f32_e32 v2, v2, v66
	s_nop 1
	v_mov_b32_dpp v18, v2 quad_perm:[1,0,3,2] row_mask:0xf bank_mask:0xf
	s_and_saveexec_b64 s[2:3], s[0:1]
	s_cbranch_execz .LBB0_1659
	s_waitcnt lgkmcnt(0)
	v_cvt_pk_bf16_f32 v2, v2, v18
	global_store_dword v[70:71], v2, off offset:192
.LBB0_1659:
	s_or_b64 exec, exec, s[2:3]
	v_rcp_f32_e32 v2, v67
	s_waitcnt lgkmcnt(0)
	v_mul_f32_e32 v18, v51, v2
	s_nop 1
	v_mov_b32_dpp v34, v18 quad_perm:[1,0,3,2] row_mask:0xf bank_mask:0xf
	s_and_saveexec_b64 s[2:3], s[0:1]
	s_cbranch_execz .LBB0_1661
	v_add_co_u32_e32 v50, vcc, 0x1000, v70
	s_waitcnt lgkmcnt(0)
	v_cvt_pk_bf16_f32 v18, v18, v34
	s_nop 0
	v_addc_co_u32_e32 v51, vcc, 0, v71, vcc
	global_store_dword v[50:51], v18, off
.LBB0_1661:
	s_or_b64 exec, exec, s[2:3]
	v_mul_f32_e32 v18, v35, v2
	s_waitcnt lgkmcnt(0)
	s_nop 1
	v_mov_b32_dpp v34, v18 quad_perm:[1,0,3,2] row_mask:0xf bank_mask:0xf
	s_and_saveexec_b64 s[2:3], s[0:1]
	s_cbranch_execz .LBB0_1663
	s_waitcnt lgkmcnt(0)
	v_cvt_pk_bf16_f32 v18, v18, v34
	v_add_co_u32_e32 v34, vcc, 0x1000, v70
	s_nop 1
	v_addc_co_u32_e32 v35, vcc, 0, v71, vcc
	global_store_dword v[34:35], v18, off offset:64
.LBB0_1663:
	s_or_b64 exec, exec, s[2:3]
	v_mul_f32_e32 v18, v19, v2
	s_nop 1
	v_mov_b32_dpp v19, v18 quad_perm:[1,0,3,2] row_mask:0xf bank_mask:0xf
	s_and_saveexec_b64 s[2:3], s[0:1]
	s_cbranch_execz .LBB0_1665
	s_waitcnt lgkmcnt(0)
	v_cvt_pk_bf16_f32 v34, v18, v19
	v_add_co_u32_e32 v18, vcc, 0x1000, v70
	s_nop 1
	v_addc_co_u32_e32 v19, vcc, 0, v71, vcc
	global_store_dword v[18:19], v34, off offset:128
.LBB0_1665:
	s_or_b64 exec, exec, s[2:3]
	v_mul_f32_e32 v2, v3, v2
	s_nop 1
	v_mov_b32_dpp v3, v2 quad_perm:[1,0,3,2] row_mask:0xf bank_mask:0xf
	s_and_saveexec_b64 s[2:3], s[0:1]
	s_cbranch_execz .LBB0_1667
	s_waitcnt lgkmcnt(0)
	v_cvt_pk_bf16_f32 v18, v2, v3
	v_add_co_u32_e32 v2, vcc, 0x1000, v70
	s_nop 1
	v_addc_co_u32_e32 v3, vcc, 0, v71, vcc
	global_store_dword v[2:3], v18, off offset:192
.LBB0_1667:
	s_or_b64 exec, exec, s[2:3]
	v_rcp_f32_e32 v2, v68
	s_waitcnt lgkmcnt(0)
	v_mul_f32_e32 v3, v52, v2
	s_nop 1
	v_mov_b32_dpp v18, v3 quad_perm:[1,0,3,2] row_mask:0xf bank_mask:0xf
	s_and_saveexec_b64 s[2:3], s[0:1]
	s_cbranch_execz .LBB0_1669
	s_waitcnt lgkmcnt(0)
	v_cvt_pk_bf16_f32 v3, v3, v18
	v_add_co_u32_e32 v18, vcc, 0x2000, v70
	s_nop 1
	v_addc_co_u32_e32 v19, vcc, 0, v71, vcc
	global_store_dword v[18:19], v3, off
.LBB0_1669:
	s_or_b64 exec, exec, s[2:3]
	v_mul_f32_e32 v3, v36, v2
	s_waitcnt lgkmcnt(0)
	s_nop 1
	v_mov_b32_dpp v18, v3 quad_perm:[1,0,3,2] row_mask:0xf bank_mask:0xf
	s_and_saveexec_b64 s[2:3], s[0:1]
	s_cbranch_execz .LBB0_1671
	s_waitcnt lgkmcnt(0)
	v_cvt_pk_bf16_f32 v3, v3, v18
	v_add_co_u32_e32 v18, vcc, 0x2000, v70
	s_nop 1
	v_addc_co_u32_e32 v19, vcc, 0, v71, vcc
	global_store_dword v[18:19], v3, off offset:64
.LBB0_1671:
	s_or_b64 exec, exec, s[2:3]
	v_mul_f32_e32 v3, v20, v2
	s_waitcnt lgkmcnt(0)
	s_nop 1
	v_mov_b32_dpp v18, v3 quad_perm:[1,0,3,2] row_mask:0xf bank_mask:0xf
	s_and_saveexec_b64 s[2:3], s[0:1]
	s_cbranch_execz .LBB0_1673
	s_waitcnt lgkmcnt(0)
	v_cvt_pk_bf16_f32 v3, v3, v18
	v_add_co_u32_e32 v18, vcc, 0x2000, v70
	s_nop 1
	v_addc_co_u32_e32 v19, vcc, 0, v71, vcc
	global_store_dword v[18:19], v3, off offset:128
.LBB0_1673:
	s_or_b64 exec, exec, s[2:3]
	v_mul_f32_e32 v2, v4, v2
	s_nop 1
	v_mov_b32_dpp v3, v2 quad_perm:[1,0,3,2] row_mask:0xf bank_mask:0xf
	s_and_saveexec_b64 s[2:3], s[0:1]
	s_cbranch_execz .LBB0_1675
	s_waitcnt lgkmcnt(0)
	v_cvt_pk_bf16_f32 v4, v2, v3
	v_add_co_u32_e32 v2, vcc, 0x2000, v70
	s_nop 1
	v_addc_co_u32_e32 v3, vcc, 0, v71, vcc
	global_store_dword v[2:3], v4, off offset:192
.LBB0_1675:
	s_or_b64 exec, exec, s[2:3]
	v_rcp_f32_e32 v2, v69
	s_waitcnt lgkmcnt(0)
	v_mul_f32_e32 v3, v53, v2
	s_nop 1
	v_mov_b32_dpp v4, v3 quad_perm:[1,0,3,2] row_mask:0xf bank_mask:0xf
	s_and_saveexec_b64 s[2:3], s[0:1]
	s_cbranch_execz .LBB0_1677
	v_add_co_u32_e32 v18, vcc, 0x3000, v70
	s_waitcnt lgkmcnt(0)
	v_cvt_pk_bf16_f32 v3, v3, v4
	s_nop 0
	v_addc_co_u32_e32 v19, vcc, 0, v71, vcc
	global_store_dword v[18:19], v3, off
.LBB0_1677:
	s_or_b64 exec, exec, s[2:3]
	v_mul_f32_e32 v3, v37, v2
	s_waitcnt lgkmcnt(0)
	s_nop 1
	v_mov_b32_dpp v4, v3 quad_perm:[1,0,3,2] row_mask:0xf bank_mask:0xf
	s_and_saveexec_b64 s[2:3], s[0:1]
	s_cbranch_execz .LBB0_1679
	v_add_co_u32_e32 v18, vcc, 0x3000, v70
	s_waitcnt lgkmcnt(0)
	v_cvt_pk_bf16_f32 v3, v3, v4
	s_nop 0
	v_addc_co_u32_e32 v19, vcc, 0, v71, vcc
	global_store_dword v[18:19], v3, off offset:64
.LBB0_1679:
	s_or_b64 exec, exec, s[2:3]
	v_mul_f32_e32 v3, v21, v2
	s_waitcnt lgkmcnt(0)
	s_nop 1
	v_mov_b32_dpp v4, v3 quad_perm:[1,0,3,2] row_mask:0xf bank_mask:0xf
	s_and_saveexec_b64 s[2:3], s[0:1]
	s_cbranch_execz .LBB0_1681
	v_add_co_u32_e32 v18, vcc, 0x3000, v70
	s_waitcnt lgkmcnt(0)
	v_cvt_pk_bf16_f32 v3, v3, v4
	s_nop 0
	v_addc_co_u32_e32 v19, vcc, 0, v71, vcc
	global_store_dword v[18:19], v3, off offset:128
.LBB0_1681:
	s_or_b64 exec, exec, s[2:3]
	v_mul_f32_e32 v2, v5, v2
	s_nop 1
	v_mov_b32_dpp v3, v2 quad_perm:[1,0,3,2] row_mask:0xf bank_mask:0xf
	s_and_saveexec_b64 s[2:3], s[0:1]
	s_cbranch_execz .LBB0_1683
	s_waitcnt lgkmcnt(0)
	v_cvt_pk_bf16_f32 v4, v2, v3
	v_add_co_u32_e32 v2, vcc, 0x3000, v70
	s_nop 1
	v_addc_co_u32_e32 v3, vcc, 0, v71, vcc
	global_store_dword v[2:3], v4, off offset:192
.LBB0_1683:
	s_or_b64 exec, exec, s[2:3]
	s_waitcnt lgkmcnt(0)
	ds_read_b128 v[2:5], v72 offset:32
	s_waitcnt lgkmcnt(0)
	v_rcp_f32_e32 v2, v2
	s_nop 0
	v_mul_f32_e32 v18, v54, v2
	s_nop 1
	v_mov_b32_dpp v19, v18 quad_perm:[1,0,3,2] row_mask:0xf bank_mask:0xf
	s_and_saveexec_b64 s[2:3], s[0:1]
	s_cbranch_execz .LBB0_1685
	s_waitcnt lgkmcnt(0)
	v_cvt_pk_bf16_f32 v20, v18, v19
	v_add_co_u32_e32 v18, vcc, 0x8000, v70
	s_nop 1
	v_addc_co_u32_e32 v19, vcc, 0, v71, vcc
	global_store_dword v[18:19], v20, off
.LBB0_1685:
	s_or_b64 exec, exec, s[2:3]
	v_mul_f32_e32 v18, v38, v2
	s_waitcnt lgkmcnt(0)
	s_nop 1
	v_mov_b32_dpp v19, v18 quad_perm:[1,0,3,2] row_mask:0xf bank_mask:0xf
	s_and_saveexec_b64 s[2:3], s[0:1]
	s_cbranch_execz .LBB0_1687
	s_waitcnt lgkmcnt(0)
	v_cvt_pk_bf16_f32 v20, v18, v19
	v_add_co_u32_e32 v18, vcc, 0x8000, v70
	s_nop 1
	v_addc_co_u32_e32 v19, vcc, 0, v71, vcc
	global_store_dword v[18:19], v20, off offset:64
.LBB0_1687:
	s_or_b64 exec, exec, s[2:3]
	v_mul_f32_e32 v18, v22, v2
	s_waitcnt lgkmcnt(0)
	s_nop 1
	v_mov_b32_dpp v19, v18 quad_perm:[1,0,3,2] row_mask:0xf bank_mask:0xf
	s_and_saveexec_b64 s[2:3], s[0:1]
	s_cbranch_execz .LBB0_1689
	s_waitcnt lgkmcnt(0)
	v_cvt_pk_bf16_f32 v20, v18, v19
	v_add_co_u32_e32 v18, vcc, 0x8000, v70
	s_nop 1
	v_addc_co_u32_e32 v19, vcc, 0, v71, vcc
	global_store_dword v[18:19], v20, off offset:128
.LBB0_1689:
	s_or_b64 exec, exec, s[2:3]
	v_mul_f32_e32 v2, v6, v2
	s_nop 1
	v_mov_b32_dpp v6, v2 quad_perm:[1,0,3,2] row_mask:0xf bank_mask:0xf
	s_and_saveexec_b64 s[2:3], s[0:1]
	s_cbranch_execz .LBB0_1691
	v_add_co_u32_e32 v18, vcc, 0x8000, v70
	s_waitcnt lgkmcnt(0)
	v_cvt_pk_bf16_f32 v2, v2, v6
	s_nop 0
	v_addc_co_u32_e32 v19, vcc, 0, v71, vcc
	global_store_dword v[18:19], v2, off offset:192
.LBB0_1691:
	s_or_b64 exec, exec, s[2:3]
	v_rcp_f32_e32 v2, v3
	s_nop 0
	v_mul_f32_e32 v3, v55, v2
	s_waitcnt lgkmcnt(0)
	s_nop 1
	v_mov_b32_dpp v6, v3 quad_perm:[1,0,3,2] row_mask:0xf bank_mask:0xf
	s_and_saveexec_b64 s[2:3], s[0:1]
	s_cbranch_execz .LBB0_1693
	v_add_co_u32_e32 v18, vcc, 0x9000, v70
	s_waitcnt lgkmcnt(0)
	v_cvt_pk_bf16_f32 v3, v3, v6
	s_nop 0
	v_addc_co_u32_e32 v19, vcc, 0, v71, vcc
	global_store_dword v[18:19], v3, off
.LBB0_1693:
	s_or_b64 exec, exec, s[2:3]
	v_mul_f32_e32 v3, v39, v2
	s_waitcnt lgkmcnt(0)
	s_nop 1
	v_mov_b32_dpp v6, v3 quad_perm:[1,0,3,2] row_mask:0xf bank_mask:0xf
	s_and_saveexec_b64 s[2:3], s[0:1]
	s_cbranch_execz .LBB0_1695
	v_add_co_u32_e32 v18, vcc, 0x9000, v70
	s_waitcnt lgkmcnt(0)
	v_cvt_pk_bf16_f32 v3, v3, v6
	s_nop 0
	v_addc_co_u32_e32 v19, vcc, 0, v71, vcc
	global_store_dword v[18:19], v3, off offset:64
.LBB0_1695:
	s_or_b64 exec, exec, s[2:3]
	v_mul_f32_e32 v3, v23, v2
	s_waitcnt lgkmcnt(0)
	s_nop 1
	v_mov_b32_dpp v6, v3 quad_perm:[1,0,3,2] row_mask:0xf bank_mask:0xf
	s_and_saveexec_b64 s[2:3], s[0:1]
	s_cbranch_execz .LBB0_1697
	v_add_co_u32_e32 v18, vcc, 0x9000, v70
	s_waitcnt lgkmcnt(0)
	v_cvt_pk_bf16_f32 v3, v3, v6
	s_nop 0
	v_addc_co_u32_e32 v19, vcc, 0, v71, vcc
	global_store_dword v[18:19], v3, off offset:128
.LBB0_1697:
	s_or_b64 exec, exec, s[2:3]
	v_mul_f32_e32 v2, v7, v2
	s_nop 1
	v_mov_b32_dpp v3, v2 quad_perm:[1,0,3,2] row_mask:0xf bank_mask:0xf
	s_and_saveexec_b64 s[2:3], s[0:1]
	s_cbranch_execz .LBB0_1699
	s_waitcnt lgkmcnt(0)
	v_cvt_pk_bf16_f32 v6, v2, v3
	v_add_co_u32_e32 v2, vcc, 0x9000, v70
	s_nop 1
	v_addc_co_u32_e32 v3, vcc, 0, v71, vcc
	global_store_dword v[2:3], v6, off offset:192
.LBB0_1699:
	s_or_b64 exec, exec, s[2:3]
	v_rcp_f32_e32 v2, v4
	s_waitcnt lgkmcnt(0)
	v_mul_f32_e32 v3, v56, v2
	s_nop 1
	v_mov_b32_dpp v4, v3 quad_perm:[1,0,3,2] row_mask:0xf bank_mask:0xf
	s_and_saveexec_b64 s[2:3], s[0:1]
	s_cbranch_execz .LBB0_1701
	v_add_co_u32_e32 v6, vcc, 0xa000, v70
	s_waitcnt lgkmcnt(0)
	v_cvt_pk_bf16_f32 v3, v3, v4
	s_nop 0
	v_addc_co_u32_e32 v7, vcc, 0, v71, vcc
	global_store_dword v[6:7], v3, off
.LBB0_1701:
	s_or_b64 exec, exec, s[2:3]
	v_mul_f32_e32 v3, v40, v2
	s_waitcnt lgkmcnt(0)
	s_nop 1
	v_mov_b32_dpp v4, v3 quad_perm:[1,0,3,2] row_mask:0xf bank_mask:0xf
	s_and_saveexec_b64 s[2:3], s[0:1]
	s_cbranch_execz .LBB0_1703
	v_add_co_u32_e32 v6, vcc, 0xa000, v70
	s_waitcnt lgkmcnt(0)
	v_cvt_pk_bf16_f32 v3, v3, v4
	s_nop 0
	v_addc_co_u32_e32 v7, vcc, 0, v71, vcc
	global_store_dword v[6:7], v3, off offset:64
.LBB0_1703:
	s_or_b64 exec, exec, s[2:3]
	v_mul_f32_e32 v3, v24, v2
	s_waitcnt lgkmcnt(0)
	s_nop 1
	v_mov_b32_dpp v4, v3 quad_perm:[1,0,3,2] row_mask:0xf bank_mask:0xf
	s_and_saveexec_b64 s[2:3], s[0:1]
	s_cbranch_execz .LBB0_1705
	v_add_co_u32_e32 v6, vcc, 0xa000, v70
	s_waitcnt lgkmcnt(0)
	v_cvt_pk_bf16_f32 v3, v3, v4
	s_nop 0
	v_addc_co_u32_e32 v7, vcc, 0, v71, vcc
	global_store_dword v[6:7], v3, off offset:128
.LBB0_1705:
	s_or_b64 exec, exec, s[2:3]
	v_mul_f32_e32 v2, v8, v2
	s_nop 1
	v_mov_b32_dpp v3, v2 quad_perm:[1,0,3,2] row_mask:0xf bank_mask:0xf
	s_and_saveexec_b64 s[2:3], s[0:1]
	s_cbranch_execz .LBB0_1707
	s_waitcnt lgkmcnt(0)
	v_cvt_pk_bf16_f32 v4, v2, v3
	v_add_co_u32_e32 v2, vcc, 0xa000, v70
	s_nop 1
	v_addc_co_u32_e32 v3, vcc, 0, v71, vcc
	global_store_dword v[2:3], v4, off offset:192
.LBB0_1707:
	s_or_b64 exec, exec, s[2:3]
	v_rcp_f32_e32 v2, v5
	s_waitcnt lgkmcnt(0)
	v_mul_f32_e32 v3, v57, v2
	s_nop 1
	v_mov_b32_dpp v4, v3 quad_perm:[1,0,3,2] row_mask:0xf bank_mask:0xf
	s_and_saveexec_b64 s[2:3], s[0:1]
	s_cbranch_execz .LBB0_1709
	s_waitcnt lgkmcnt(0)
	v_cvt_pk_bf16_f32 v3, v3, v4
	v_add_co_u32_e32 v4, vcc, 0xb000, v70
	s_nop 1
	v_addc_co_u32_e32 v5, vcc, 0, v71, vcc
	global_store_dword v[4:5], v3, off
.LBB0_1709:
	s_or_b64 exec, exec, s[2:3]
	v_mul_f32_e32 v3, v41, v2
	s_waitcnt lgkmcnt(0)
	s_nop 1
	v_mov_b32_dpp v4, v3 quad_perm:[1,0,3,2] row_mask:0xf bank_mask:0xf
	s_and_saveexec_b64 s[2:3], s[0:1]
	s_cbranch_execz .LBB0_1711
	s_waitcnt lgkmcnt(0)
	v_cvt_pk_bf16_f32 v3, v3, v4
	v_add_co_u32_e32 v4, vcc, 0xb000, v70
	s_nop 1
	v_addc_co_u32_e32 v5, vcc, 0, v71, vcc
	global_store_dword v[4:5], v3, off offset:64
.LBB0_1711:
	s_or_b64 exec, exec, s[2:3]
	v_mul_f32_e32 v3, v25, v2
	s_waitcnt lgkmcnt(0)
	s_nop 1
	v_mov_b32_dpp v4, v3 quad_perm:[1,0,3,2] row_mask:0xf bank_mask:0xf
	s_and_saveexec_b64 s[2:3], s[0:1]
	s_cbranch_execz .LBB0_1713
	s_waitcnt lgkmcnt(0)
	v_cvt_pk_bf16_f32 v3, v3, v4
	v_add_co_u32_e32 v4, vcc, 0xb000, v70
	s_nop 1
	v_addc_co_u32_e32 v5, vcc, 0, v71, vcc
	global_store_dword v[4:5], v3, off offset:128
.LBB0_1713:
	s_or_b64 exec, exec, s[2:3]
	v_mul_f32_e32 v2, v9, v2
	s_nop 1
	v_mov_b32_dpp v3, v2 quad_perm:[1,0,3,2] row_mask:0xf bank_mask:0xf
	s_and_saveexec_b64 s[2:3], s[0:1]
	s_cbranch_execz .LBB0_1715
	s_waitcnt lgkmcnt(0)
	v_cvt_pk_bf16_f32 v4, v2, v3
	v_add_co_u32_e32 v2, vcc, 0xb000, v70
	s_nop 1
	v_addc_co_u32_e32 v3, vcc, 0, v71, vcc
	global_store_dword v[2:3], v4, off offset:192
.LBB0_1715:
	s_or_b64 exec, exec, s[2:3]
	s_waitcnt lgkmcnt(0)
	ds_read_b128 v[2:5], v72 offset:64
	s_waitcnt lgkmcnt(0)
	v_rcp_f32_e32 v2, v2
	s_nop 0
	v_mul_f32_e32 v6, v58, v2
	s_nop 1
	v_mov_b32_dpp v7, v6 quad_perm:[1,0,3,2] row_mask:0xf bank_mask:0xf
	s_and_saveexec_b64 s[2:3], s[0:1]
	s_cbranch_execz .LBB0_1717
	s_waitcnt lgkmcnt(0)
	v_cvt_pk_bf16_f32 v8, v6, v7
	v_add_co_u32_e32 v6, vcc, 0x10000, v70
	s_nop 1
	v_addc_co_u32_e32 v7, vcc, 0, v71, vcc
	global_store_dword v[6:7], v8, off
.LBB0_1717:
	s_or_b64 exec, exec, s[2:3]
	v_mul_f32_e32 v6, v42, v2
	s_waitcnt lgkmcnt(0)
	s_nop 1
	v_mov_b32_dpp v7, v6 quad_perm:[1,0,3,2] row_mask:0xf bank_mask:0xf
	s_and_saveexec_b64 s[2:3], s[0:1]
	s_cbranch_execz .LBB0_1719
	s_waitcnt lgkmcnt(0)
	v_cvt_pk_bf16_f32 v8, v6, v7
	v_add_co_u32_e32 v6, vcc, 0x10000, v70
	s_nop 1
	v_addc_co_u32_e32 v7, vcc, 0, v71, vcc
	global_store_dword v[6:7], v8, off offset:64
.LBB0_1719:
	s_or_b64 exec, exec, s[2:3]
	v_mul_f32_e32 v6, v26, v2
	s_waitcnt lgkmcnt(0)
	s_nop 1
	v_mov_b32_dpp v7, v6 quad_perm:[1,0,3,2] row_mask:0xf bank_mask:0xf
	s_and_saveexec_b64 s[2:3], s[0:1]
	s_cbranch_execz .LBB0_1721
	s_waitcnt lgkmcnt(0)
	v_cvt_pk_bf16_f32 v8, v6, v7
	v_add_co_u32_e32 v6, vcc, 0x10000, v70
	s_nop 1
	v_addc_co_u32_e32 v7, vcc, 0, v71, vcc
	global_store_dword v[6:7], v8, off offset:128
.LBB0_1721:
	s_or_b64 exec, exec, s[2:3]
	v_mul_f32_e32 v2, v10, v2
	s_nop 1
	v_mov_b32_dpp v6, v2 quad_perm:[1,0,3,2] row_mask:0xf bank_mask:0xf
	s_and_saveexec_b64 s[2:3], s[0:1]
	s_cbranch_execz .LBB0_1723
	s_waitcnt lgkmcnt(0)
	v_cvt_pk_bf16_f32 v2, v2, v6
	v_add_co_u32_e32 v6, vcc, 0x10000, v70
	s_nop 1
	v_addc_co_u32_e32 v7, vcc, 0, v71, vcc
	global_store_dword v[6:7], v2, off offset:192
.LBB0_1723:
	s_or_b64 exec, exec, s[2:3]
	v_rcp_f32_e32 v2, v3
	s_nop 0
	v_mul_f32_e32 v3, v59, v2
	s_waitcnt lgkmcnt(0)
	s_nop 1
	v_mov_b32_dpp v6, v3 quad_perm:[1,0,3,2] row_mask:0xf bank_mask:0xf
	s_and_saveexec_b64 s[2:3], s[0:1]
	s_cbranch_execz .LBB0_1725
	s_waitcnt lgkmcnt(0)
	v_cvt_pk_bf16_f32 v3, v3, v6
	v_add_co_u32_e32 v6, vcc, 0x11000, v70
	s_nop 1
	v_addc_co_u32_e32 v7, vcc, 0, v71, vcc
	global_store_dword v[6:7], v3, off
.LBB0_1725:
	s_or_b64 exec, exec, s[2:3]
	v_mul_f32_e32 v3, v43, v2
	s_waitcnt lgkmcnt(0)
	s_nop 1
	v_mov_b32_dpp v6, v3 quad_perm:[1,0,3,2] row_mask:0xf bank_mask:0xf
	s_and_saveexec_b64 s[2:3], s[0:1]
	s_cbranch_execz .LBB0_1727
	s_waitcnt lgkmcnt(0)
	v_cvt_pk_bf16_f32 v3, v3, v6
	v_add_co_u32_e32 v6, vcc, 0x11000, v70
	s_nop 1
	v_addc_co_u32_e32 v7, vcc, 0, v71, vcc
	global_store_dword v[6:7], v3, off offset:64
.LBB0_1727:
	s_or_b64 exec, exec, s[2:3]
	v_mul_f32_e32 v3, v27, v2
	s_waitcnt lgkmcnt(0)
	s_nop 1
	v_mov_b32_dpp v6, v3 quad_perm:[1,0,3,2] row_mask:0xf bank_mask:0xf
	s_and_saveexec_b64 s[2:3], s[0:1]
	s_cbranch_execz .LBB0_1729
	s_waitcnt lgkmcnt(0)
	v_cvt_pk_bf16_f32 v3, v3, v6
	v_add_co_u32_e32 v6, vcc, 0x11000, v70
	s_nop 1
	v_addc_co_u32_e32 v7, vcc, 0, v71, vcc
	global_store_dword v[6:7], v3, off offset:128
.LBB0_1729:
	s_or_b64 exec, exec, s[2:3]
	v_mul_f32_e32 v2, v11, v2
	s_nop 1
	v_mov_b32_dpp v3, v2 quad_perm:[1,0,3,2] row_mask:0xf bank_mask:0xf
	s_and_saveexec_b64 s[2:3], s[0:1]
	s_cbranch_execz .LBB0_1731
	s_waitcnt lgkmcnt(0)
	v_cvt_pk_bf16_f32 v6, v2, v3
	v_add_co_u32_e32 v2, vcc, 0x11000, v70
	s_nop 1
	v_addc_co_u32_e32 v3, vcc, 0, v71, vcc
	global_store_dword v[2:3], v6, off offset:192
.LBB0_1731:
	s_or_b64 exec, exec, s[2:3]
	v_rcp_f32_e32 v2, v4
	s_waitcnt lgkmcnt(0)
	v_mul_f32_e32 v3, v60, v2
	s_nop 1
	v_mov_b32_dpp v4, v3 quad_perm:[1,0,3,2] row_mask:0xf bank_mask:0xf
	s_and_saveexec_b64 s[2:3], s[0:1]
	s_cbranch_execz .LBB0_1733
	v_add_co_u32_e32 v6, vcc, 0x12000, v70
	s_waitcnt lgkmcnt(0)
	v_cvt_pk_bf16_f32 v3, v3, v4
	s_nop 0
	v_addc_co_u32_e32 v7, vcc, 0, v71, vcc
	global_store_dword v[6:7], v3, off
.LBB0_1733:
	s_or_b64 exec, exec, s[2:3]
	v_mul_f32_e32 v3, v44, v2
	s_waitcnt lgkmcnt(0)
	s_nop 1
	v_mov_b32_dpp v4, v3 quad_perm:[1,0,3,2] row_mask:0xf bank_mask:0xf
	s_and_saveexec_b64 s[2:3], s[0:1]
	s_cbranch_execz .LBB0_1735
	v_add_co_u32_e32 v6, vcc, 0x12000, v70
	s_waitcnt lgkmcnt(0)
	v_cvt_pk_bf16_f32 v3, v3, v4
	s_nop 0
	v_addc_co_u32_e32 v7, vcc, 0, v71, vcc
	global_store_dword v[6:7], v3, off offset:64
.LBB0_1735:
	s_or_b64 exec, exec, s[2:3]
	v_mul_f32_e32 v3, v28, v2
	s_waitcnt lgkmcnt(0)
	s_nop 1
	v_mov_b32_dpp v4, v3 quad_perm:[1,0,3,2] row_mask:0xf bank_mask:0xf
	s_and_saveexec_b64 s[2:3], s[0:1]
	s_cbranch_execz .LBB0_1737
	v_add_co_u32_e32 v6, vcc, 0x12000, v70
	s_waitcnt lgkmcnt(0)
	v_cvt_pk_bf16_f32 v3, v3, v4
	s_nop 0
	v_addc_co_u32_e32 v7, vcc, 0, v71, vcc
	global_store_dword v[6:7], v3, off offset:128
.LBB0_1737:
	s_or_b64 exec, exec, s[2:3]
	v_mul_f32_e32 v2, v12, v2
	s_nop 1
	v_mov_b32_dpp v3, v2 quad_perm:[1,0,3,2] row_mask:0xf bank_mask:0xf
	s_and_saveexec_b64 s[2:3], s[0:1]
	s_cbranch_execz .LBB0_1739
	s_waitcnt lgkmcnt(0)
	v_cvt_pk_bf16_f32 v4, v2, v3
	v_add_co_u32_e32 v2, vcc, 0x12000, v70
	s_nop 1
	v_addc_co_u32_e32 v3, vcc, 0, v71, vcc
	global_store_dword v[2:3], v4, off offset:192
.LBB0_1739:
	s_or_b64 exec, exec, s[2:3]
	v_rcp_f32_e32 v2, v5
	s_waitcnt lgkmcnt(0)
	v_mul_f32_e32 v3, v61, v2
	s_nop 1
	v_mov_b32_dpp v4, v3 quad_perm:[1,0,3,2] row_mask:0xf bank_mask:0xf
	s_and_saveexec_b64 s[2:3], s[0:1]
	s_cbranch_execz .LBB0_1741
	s_waitcnt lgkmcnt(0)
	v_cvt_pk_bf16_f32 v3, v3, v4
	v_add_co_u32_e32 v4, vcc, 0x13000, v70
	s_nop 1
	v_addc_co_u32_e32 v5, vcc, 0, v71, vcc
	global_store_dword v[4:5], v3, off
.LBB0_1741:
	s_or_b64 exec, exec, s[2:3]
	v_mul_f32_e32 v3, v45, v2
	s_waitcnt lgkmcnt(0)
	s_nop 1
	v_mov_b32_dpp v4, v3 quad_perm:[1,0,3,2] row_mask:0xf bank_mask:0xf
	s_and_saveexec_b64 s[2:3], s[0:1]
	s_cbranch_execz .LBB0_1743
	s_waitcnt lgkmcnt(0)
	v_cvt_pk_bf16_f32 v3, v3, v4
	v_add_co_u32_e32 v4, vcc, 0x13000, v70
	s_nop 1
	v_addc_co_u32_e32 v5, vcc, 0, v71, vcc
	global_store_dword v[4:5], v3, off offset:64
.LBB0_1743:
	s_or_b64 exec, exec, s[2:3]
	v_mul_f32_e32 v3, v29, v2
	s_waitcnt lgkmcnt(0)
	s_nop 1
	v_mov_b32_dpp v4, v3 quad_perm:[1,0,3,2] row_mask:0xf bank_mask:0xf
	s_and_saveexec_b64 s[2:3], s[0:1]
	s_cbranch_execz .LBB0_1745
	s_waitcnt lgkmcnt(0)
	v_cvt_pk_bf16_f32 v3, v3, v4
	v_add_co_u32_e32 v4, vcc, 0x13000, v70
	s_nop 1
	v_addc_co_u32_e32 v5, vcc, 0, v71, vcc
	global_store_dword v[4:5], v3, off offset:128
.LBB0_1745:
	s_or_b64 exec, exec, s[2:3]
	v_mul_f32_e32 v2, v13, v2
	s_nop 1
	v_mov_b32_dpp v3, v2 quad_perm:[1,0,3,2] row_mask:0xf bank_mask:0xf
	s_and_saveexec_b64 s[2:3], s[0:1]
	s_cbranch_execz .LBB0_1747
	s_waitcnt lgkmcnt(0)
	v_cvt_pk_bf16_f32 v4, v2, v3
	v_add_co_u32_e32 v2, vcc, 0x13000, v70
	s_nop 1
	v_addc_co_u32_e32 v3, vcc, 0, v71, vcc
	global_store_dword v[2:3], v4, off offset:192
.LBB0_1747:
	s_or_b64 exec, exec, s[2:3]
	s_waitcnt lgkmcnt(0)
	ds_read_b128 v[2:5], v72 offset:96
	s_waitcnt lgkmcnt(0)
	v_rcp_f32_e32 v2, v2
	s_nop 0
	v_mul_f32_e32 v6, v62, v2
	s_nop 1
	v_mov_b32_dpp v7, v6 quad_perm:[1,0,3,2] row_mask:0xf bank_mask:0xf
	s_and_saveexec_b64 s[2:3], s[0:1]
	s_cbranch_execz .LBB0_1749
	s_waitcnt lgkmcnt(0)
	v_cvt_pk_bf16_f32 v8, v6, v7
	v_add_co_u32_e32 v6, vcc, 0x18000, v70
	s_nop 1
	v_addc_co_u32_e32 v7, vcc, 0, v71, vcc
	global_store_dword v[6:7], v8, off
.LBB0_1749:
	s_or_b64 exec, exec, s[2:3]
	v_mul_f32_e32 v6, v46, v2
	s_waitcnt lgkmcnt(0)
	s_nop 1
	v_mov_b32_dpp v7, v6 quad_perm:[1,0,3,2] row_mask:0xf bank_mask:0xf
	s_and_saveexec_b64 s[2:3], s[0:1]
	s_cbranch_execz .LBB0_1751
	s_waitcnt lgkmcnt(0)
	v_cvt_pk_bf16_f32 v8, v6, v7
	v_add_co_u32_e32 v6, vcc, 0x18000, v70
	s_nop 1
	v_addc_co_u32_e32 v7, vcc, 0, v71, vcc
	global_store_dword v[6:7], v8, off offset:64
.LBB0_1751:
	s_or_b64 exec, exec, s[2:3]
	v_mul_f32_e32 v6, v30, v2
	s_waitcnt lgkmcnt(0)
	s_nop 1
	v_mov_b32_dpp v7, v6 quad_perm:[1,0,3,2] row_mask:0xf bank_mask:0xf
	s_and_saveexec_b64 s[2:3], s[0:1]
	s_cbranch_execz .LBB0_1753
	s_waitcnt lgkmcnt(0)
	v_cvt_pk_bf16_f32 v8, v6, v7
	v_add_co_u32_e32 v6, vcc, 0x18000, v70
	s_nop 1
	v_addc_co_u32_e32 v7, vcc, 0, v71, vcc
	global_store_dword v[6:7], v8, off offset:128
.LBB0_1753:
	s_or_b64 exec, exec, s[2:3]
	v_mul_f32_e32 v2, v14, v2
	s_nop 1
	v_mov_b32_dpp v6, v2 quad_perm:[1,0,3,2] row_mask:0xf bank_mask:0xf
	s_and_saveexec_b64 s[2:3], s[0:1]
	s_cbranch_execz .LBB0_1755
	s_waitcnt lgkmcnt(0)
	v_cvt_pk_bf16_f32 v2, v2, v6
	v_add_co_u32_e32 v6, vcc, 0x18000, v70
	s_nop 1
	v_addc_co_u32_e32 v7, vcc, 0, v71, vcc
	global_store_dword v[6:7], v2, off offset:192
.LBB0_1755:
	s_or_b64 exec, exec, s[2:3]
	v_rcp_f32_e32 v2, v3
	s_nop 0
	v_mul_f32_e32 v3, v63, v2
	s_waitcnt lgkmcnt(0)
	s_nop 1
	v_mov_b32_dpp v6, v3 quad_perm:[1,0,3,2] row_mask:0xf bank_mask:0xf
	s_and_saveexec_b64 s[2:3], s[0:1]
	s_cbranch_execz .LBB0_1757
	s_waitcnt lgkmcnt(0)
	v_cvt_pk_bf16_f32 v3, v3, v6
	v_add_co_u32_e32 v6, vcc, 0x19000, v70
	s_nop 1
	v_addc_co_u32_e32 v7, vcc, 0, v71, vcc
	global_store_dword v[6:7], v3, off
.LBB0_1757:
	s_or_b64 exec, exec, s[2:3]
	v_mul_f32_e32 v3, v47, v2
	s_waitcnt lgkmcnt(0)
	s_nop 1
	v_mov_b32_dpp v6, v3 quad_perm:[1,0,3,2] row_mask:0xf bank_mask:0xf
	s_and_saveexec_b64 s[2:3], s[0:1]
	s_cbranch_execz .LBB0_1759
	s_waitcnt lgkmcnt(0)
	v_cvt_pk_bf16_f32 v3, v3, v6
	v_add_co_u32_e32 v6, vcc, 0x19000, v70
	s_nop 1
	v_addc_co_u32_e32 v7, vcc, 0, v71, vcc
	global_store_dword v[6:7], v3, off offset:64
.LBB0_1759:
	s_or_b64 exec, exec, s[2:3]
	v_mul_f32_e32 v3, v31, v2
	s_waitcnt lgkmcnt(0)
	s_nop 1
	v_mov_b32_dpp v6, v3 quad_perm:[1,0,3,2] row_mask:0xf bank_mask:0xf
	s_and_saveexec_b64 s[2:3], s[0:1]
	s_cbranch_execz .LBB0_1761
	s_waitcnt lgkmcnt(0)
	v_cvt_pk_bf16_f32 v3, v3, v6
	v_add_co_u32_e32 v6, vcc, 0x19000, v70
	s_nop 1
	v_addc_co_u32_e32 v7, vcc, 0, v71, vcc
	global_store_dword v[6:7], v3, off offset:128
.LBB0_1761:
	s_or_b64 exec, exec, s[2:3]
	v_mul_f32_e32 v2, v15, v2
	s_nop 1
	v_mov_b32_dpp v3, v2 quad_perm:[1,0,3,2] row_mask:0xf bank_mask:0xf
	s_and_saveexec_b64 s[2:3], s[0:1]
	s_cbranch_execz .LBB0_1763
	s_waitcnt lgkmcnt(0)
	v_cvt_pk_bf16_f32 v6, v2, v3
	v_add_co_u32_e32 v2, vcc, 0x19000, v70
	s_nop 1
	v_addc_co_u32_e32 v3, vcc, 0, v71, vcc
	global_store_dword v[2:3], v6, off offset:192
.LBB0_1763:
	s_or_b64 exec, exec, s[2:3]
	v_rcp_f32_e32 v2, v4
	s_waitcnt lgkmcnt(0)
	v_mul_f32_e32 v3, v64, v2
	s_nop 1
	v_mov_b32_dpp v4, v3 quad_perm:[1,0,3,2] row_mask:0xf bank_mask:0xf
	s_and_saveexec_b64 s[2:3], s[0:1]
	s_cbranch_execz .LBB0_1765
	v_add_co_u32_e32 v6, vcc, 0x1a000, v70
	s_waitcnt lgkmcnt(0)
	v_cvt_pk_bf16_f32 v3, v3, v4
	s_nop 0
	v_addc_co_u32_e32 v7, vcc, 0, v71, vcc
	global_store_dword v[6:7], v3, off
.LBB0_1765:
	s_or_b64 exec, exec, s[2:3]
	v_mul_f32_e32 v3, v48, v2
	s_waitcnt lgkmcnt(0)
	s_nop 1
	v_mov_b32_dpp v4, v3 quad_perm:[1,0,3,2] row_mask:0xf bank_mask:0xf
	s_and_saveexec_b64 s[2:3], s[0:1]
	s_cbranch_execz .LBB0_1767
	v_add_co_u32_e32 v6, vcc, 0x1a000, v70
	s_waitcnt lgkmcnt(0)
	v_cvt_pk_bf16_f32 v3, v3, v4
	s_nop 0
	v_addc_co_u32_e32 v7, vcc, 0, v71, vcc
	global_store_dword v[6:7], v3, off offset:64
.LBB0_1767:
	s_or_b64 exec, exec, s[2:3]
	v_mul_f32_e32 v3, v32, v2
	s_waitcnt lgkmcnt(0)
	s_nop 1
	v_mov_b32_dpp v4, v3 quad_perm:[1,0,3,2] row_mask:0xf bank_mask:0xf
	s_and_saveexec_b64 s[2:3], s[0:1]
	s_cbranch_execz .LBB0_1769
	v_add_co_u32_e32 v6, vcc, 0x1a000, v70
	s_waitcnt lgkmcnt(0)
	v_cvt_pk_bf16_f32 v3, v3, v4
	s_nop 0
	v_addc_co_u32_e32 v7, vcc, 0, v71, vcc
	global_store_dword v[6:7], v3, off offset:128
.LBB0_1769:
	s_or_b64 exec, exec, s[2:3]
	v_mul_f32_e32 v2, v16, v2
	s_nop 1
	v_mov_b32_dpp v3, v2 quad_perm:[1,0,3,2] row_mask:0xf bank_mask:0xf
	s_and_saveexec_b64 s[2:3], s[0:1]
	s_cbranch_execz .LBB0_1771
	s_waitcnt lgkmcnt(0)
	v_cvt_pk_bf16_f32 v4, v2, v3
	v_add_co_u32_e32 v2, vcc, 0x1a000, v70
	s_nop 1
	v_addc_co_u32_e32 v3, vcc, 0, v71, vcc
	global_store_dword v[2:3], v4, off offset:192
.LBB0_1771:
	s_or_b64 exec, exec, s[2:3]
	v_rcp_f32_e32 v2, v5
	s_waitcnt lgkmcnt(0)
	v_mul_f32_e32 v3, v65, v2
	s_nop 1
	v_mov_b32_dpp v4, v3 quad_perm:[1,0,3,2] row_mask:0xf bank_mask:0xf
	s_and_saveexec_b64 s[2:3], s[0:1]
	s_cbranch_execz .LBB0_1773
	s_waitcnt lgkmcnt(0)
	v_cvt_pk_bf16_f32 v3, v3, v4
	v_add_co_u32_e32 v4, vcc, 0x1b000, v70
	s_nop 1
	v_addc_co_u32_e32 v5, vcc, 0, v71, vcc
	global_store_dword v[4:5], v3, off
.LBB0_1773:
	s_or_b64 exec, exec, s[2:3]
	v_mul_f32_e32 v3, v49, v2
	s_waitcnt lgkmcnt(0)
	s_nop 1
	v_mov_b32_dpp v4, v3 quad_perm:[1,0,3,2] row_mask:0xf bank_mask:0xf
	s_and_saveexec_b64 s[2:3], s[0:1]
	s_cbranch_execz .LBB0_1775
	s_waitcnt lgkmcnt(0)
	v_cvt_pk_bf16_f32 v3, v3, v4
	v_add_co_u32_e32 v4, vcc, 0x1b000, v70
	s_nop 1
	v_addc_co_u32_e32 v5, vcc, 0, v71, vcc
	global_store_dword v[4:5], v3, off offset:64
.LBB0_1775:
	s_or_b64 exec, exec, s[2:3]
	v_mul_f32_e32 v3, v33, v2
	s_waitcnt lgkmcnt(0)
	s_nop 1
	v_mov_b32_dpp v4, v3 quad_perm:[1,0,3,2] row_mask:0xf bank_mask:0xf
	s_and_saveexec_b64 s[2:3], s[0:1]
	s_cbranch_execz .LBB0_1777
	s_waitcnt lgkmcnt(0)
	v_cvt_pk_bf16_f32 v3, v3, v4
	v_add_co_u32_e32 v4, vcc, 0x1b000, v70
	s_nop 1
	v_addc_co_u32_e32 v5, vcc, 0, v71, vcc
	global_store_dword v[4:5], v3, off offset:128
.LBB0_1777:
	s_or_b64 exec, exec, s[2:3]
	v_mul_f32_e32 v2, v17, v2
	s_nop 1
	v_mov_b32_dpp v1, v2 quad_perm:[1,0,3,2] row_mask:0xf bank_mask:0xf
	s_and_saveexec_b64 s[2:3], s[0:1]
	s_cbranch_execz .LBB0_1474
	s_waitcnt lgkmcnt(0)
	v_cvt_pk_bf16_f32 v1, v2, v1
	v_add_co_u32_e32 v2, vcc, 0x1b000, v70
	s_nop 1
	v_addc_co_u32_e32 v3, vcc, 0, v71, vcc
	global_store_dword v[2:3], v1, off offset:192
	s_branch .LBB0_1474

.LBB0_1917:
	s_and_saveexec_b64 s[0:1], s[2:3]
	ds_write_b32 v176, v189
	s_or_b64 exec, exec, s[0:1]
	v_xor_b32_e32 v1, 1, v215
	v_add_u32_e32 v66, 64, v81
	s_lshl_b64 s[0:1], s[76:77], 23
	v_readlane_b32 s2, v254, 9
	v_cmp_lt_i32_e32 vcc, v1, v66
	s_add_u32 s0, s2, s0
	v_readlane_b32 s2, v254, 11
	v_cndmask_b32_e32 v1, v215, v1, vcc
	s_addc_u32 s1, s2, s1
	s_lshl_b32 s2, s79, 1
	v_lshlrev_b32_e32 v81, 2, v1
	v_and_b32_e32 v1, 1, v171
	s_add_u32 s81, s0, s2
	s_waitcnt lgkmcnt(0)
	v_cmp_eq_u32_e64 s[2:3], 0, v1
	v_add_u32_e32 v1, s85, v164
	ds_read_b128 v[66:69], v1
	s_addc_u32 s80, s1, 0
	s_ashr_i32 s79, s78, 31
	s_lshl_b64 s[0:1], s[78:79], 12
	s_add_u32 s0, s81, s0
	s_waitcnt lgkmcnt(0)
	v_rcp_f32_e32 v66, v66
	s_addc_u32 s1, s80, s1
	v_lshlrev_b32_e32 v86, 1, v172
	v_lshl_add_u64 v[70:71], s[0:1], 0, v[86:87]
	v_mul_f32_e32 v50, v50, v66
	s_nop 1
	v_mov_b32_dpp v72, v50 quad_perm:[1,0,3,2] row_mask:0xf bank_mask:0xf
	v_lshlrev_b32_e32 v86, 14, v170
	v_lshl_add_u64 v[70:71], v[70:71], 0, v[86:87]
	s_and_saveexec_b64 s[0:1], s[2:3]
	s_cbranch_execz .LBB0_1921
	s_waitcnt lgkmcnt(0)
	v_cvt_pk_bf16_f32 v50, v50, v72
	global_store_dword v[70:71], v50, off
.LBB0_1921:
	s_or_b64 exec, exec, s[0:1]
	v_mul_f32_e32 v34, v34, v66
	s_nop 1
	v_mov_b32_dpp v50, v34 quad_perm:[1,0,3,2] row_mask:0xf bank_mask:0xf
	s_and_saveexec_b64 s[0:1], s[2:3]
	s_cbranch_execz .LBB0_1923
	s_waitcnt lgkmcnt(0)
	v_cvt_pk_bf16_f32 v34, v34, v50
	global_store_dword v[70:71], v34, off offset:64
.LBB0_1923:
	s_or_b64 exec, exec, s[0:1]
	v_mul_f32_e32 v18, v18, v66
	s_nop 1
	v_mov_b32_dpp v34, v18 quad_perm:[1,0,3,2] row_mask:0xf bank_mask:0xf
	s_and_saveexec_b64 s[0:1], s[2:3]
	s_cbranch_execz .LBB0_1925
	s_waitcnt lgkmcnt(0)
	v_cvt_pk_bf16_f32 v18, v18, v34
	global_store_dword v[70:71], v18, off offset:128
.LBB0_1925:
	s_or_b64 exec, exec, s[0:1]
	v_mul_f32_e32 v2, v2, v66
	s_nop 1
	v_mov_b32_dpp v18, v2 quad_perm:[1,0,3,2] row_mask:0xf bank_mask:0xf
	s_and_saveexec_b64 s[0:1], s[2:3]
	s_cbranch_execz .LBB0_1927
	s_waitcnt lgkmcnt(0)
	v_cvt_pk_bf16_f32 v2, v2, v18
	global_store_dword v[70:71], v2, off offset:192
.LBB0_1927:
	s_or_b64 exec, exec, s[0:1]
	v_rcp_f32_e32 v2, v67
	s_waitcnt lgkmcnt(0)
	v_mul_f32_e32 v18, v51, v2
	s_nop 1
	v_mov_b32_dpp v34, v18 quad_perm:[1,0,3,2] row_mask:0xf bank_mask:0xf
	s_and_saveexec_b64 s[0:1], s[2:3]
	s_cbranch_execz .LBB0_1929
	v_add_co_u32_e32 v50, vcc, 0x1000, v70
	s_waitcnt lgkmcnt(0)
	v_cvt_pk_bf16_f32 v18, v18, v34
	s_nop 0
	v_addc_co_u32_e32 v51, vcc, 0, v71, vcc
	global_store_dword v[50:51], v18, off
.LBB0_1929:
	s_or_b64 exec, exec, s[0:1]
	v_mul_f32_e32 v18, v35, v2
	s_waitcnt lgkmcnt(0)
	s_nop 1
	v_mov_b32_dpp v34, v18 quad_perm:[1,0,3,2] row_mask:0xf bank_mask:0xf
	s_and_saveexec_b64 s[0:1], s[2:3]
	s_cbranch_execz .LBB0_1931
	s_waitcnt lgkmcnt(0)
	v_cvt_pk_bf16_f32 v18, v18, v34
	v_add_co_u32_e32 v34, vcc, 0x1000, v70
	s_nop 1
	v_addc_co_u32_e32 v35, vcc, 0, v71, vcc
	global_store_dword v[34:35], v18, off offset:64
.LBB0_1931:
	s_or_b64 exec, exec, s[0:1]
	v_mul_f32_e32 v18, v19, v2
	s_nop 1
	v_mov_b32_dpp v19, v18 quad_perm:[1,0,3,2] row_mask:0xf bank_mask:0xf
	s_and_saveexec_b64 s[0:1], s[2:3]
	s_cbranch_execz .LBB0_1933
	s_waitcnt lgkmcnt(0)
	v_cvt_pk_bf16_f32 v34, v18, v19
	v_add_co_u32_e32 v18, vcc, 0x1000, v70
	s_nop 1
	v_addc_co_u32_e32 v19, vcc, 0, v71, vcc
	global_store_dword v[18:19], v34, off offset:128
.LBB0_1933:
	s_or_b64 exec, exec, s[0:1]
	v_mul_f32_e32 v2, v3, v2
	s_nop 1
	v_mov_b32_dpp v3, v2 quad_perm:[1,0,3,2] row_mask:0xf bank_mask:0xf
	s_and_saveexec_b64 s[0:1], s[2:3]
	s_cbranch_execz .LBB0_1935
	s_waitcnt lgkmcnt(0)
	v_cvt_pk_bf16_f32 v18, v2, v3
	v_add_co_u32_e32 v2, vcc, 0x1000, v70
	s_nop 1
	v_addc_co_u32_e32 v3, vcc, 0, v71, vcc
	global_store_dword v[2:3], v18, off offset:192
.LBB0_1935:
	s_or_b64 exec, exec, s[0:1]
	v_rcp_f32_e32 v2, v68
	s_waitcnt lgkmcnt(0)
	v_mul_f32_e32 v3, v52, v2
	s_nop 1
	v_mov_b32_dpp v18, v3 quad_perm:[1,0,3,2] row_mask:0xf bank_mask:0xf
	s_and_saveexec_b64 s[0:1], s[2:3]
	s_cbranch_execz .LBB0_1937
	s_waitcnt lgkmcnt(0)
	v_cvt_pk_bf16_f32 v3, v3, v18
	v_add_co_u32_e32 v18, vcc, 0x2000, v70
	s_nop 1
	v_addc_co_u32_e32 v19, vcc, 0, v71, vcc
	global_store_dword v[18:19], v3, off
.LBB0_1937:
	s_or_b64 exec, exec, s[0:1]
	v_mul_f32_e32 v3, v36, v2
	s_waitcnt lgkmcnt(0)
	s_nop 1
	v_mov_b32_dpp v18, v3 quad_perm:[1,0,3,2] row_mask:0xf bank_mask:0xf
	s_and_saveexec_b64 s[0:1], s[2:3]
	s_cbranch_execz .LBB0_1939
	s_waitcnt lgkmcnt(0)
	v_cvt_pk_bf16_f32 v3, v3, v18
	v_add_co_u32_e32 v18, vcc, 0x2000, v70
	s_nop 1
	v_addc_co_u32_e32 v19, vcc, 0, v71, vcc
	global_store_dword v[18:19], v3, off offset:64
.LBB0_1939:
	s_or_b64 exec, exec, s[0:1]
	v_mul_f32_e32 v3, v20, v2
	s_waitcnt lgkmcnt(0)
	s_nop 1
	v_mov_b32_dpp v18, v3 quad_perm:[1,0,3,2] row_mask:0xf bank_mask:0xf
	s_and_saveexec_b64 s[0:1], s[2:3]
	s_cbranch_execz .LBB0_1941
	s_waitcnt lgkmcnt(0)
	v_cvt_pk_bf16_f32 v3, v3, v18
	v_add_co_u32_e32 v18, vcc, 0x2000, v70
	s_nop 1
	v_addc_co_u32_e32 v19, vcc, 0, v71, vcc
	global_store_dword v[18:19], v3, off offset:128
.LBB0_1941:
	s_or_b64 exec, exec, s[0:1]
	v_mul_f32_e32 v2, v4, v2
	s_nop 1
	v_mov_b32_dpp v3, v2 quad_perm:[1,0,3,2] row_mask:0xf bank_mask:0xf
	s_and_saveexec_b64 s[0:1], s[2:3]
	s_cbranch_execz .LBB0_1943
	s_waitcnt lgkmcnt(0)
	v_cvt_pk_bf16_f32 v4, v2, v3
	v_add_co_u32_e32 v2, vcc, 0x2000, v70
	s_nop 1
	v_addc_co_u32_e32 v3, vcc, 0, v71, vcc
	global_store_dword v[2:3], v4, off offset:192
.LBB0_1943:
	s_or_b64 exec, exec, s[0:1]
	v_rcp_f32_e32 v2, v69
	s_waitcnt lgkmcnt(0)
	v_mul_f32_e32 v3, v53, v2
	s_nop 1
	v_mov_b32_dpp v4, v3 quad_perm:[1,0,3,2] row_mask:0xf bank_mask:0xf
	s_and_saveexec_b64 s[0:1], s[2:3]
	s_cbranch_execz .LBB0_1945
	v_add_co_u32_e32 v18, vcc, 0x3000, v70
	s_waitcnt lgkmcnt(0)
	v_cvt_pk_bf16_f32 v3, v3, v4
	s_nop 0
	v_addc_co_u32_e32 v19, vcc, 0, v71, vcc
	global_store_dword v[18:19], v3, off
.LBB0_1945:
	s_or_b64 exec, exec, s[0:1]
	v_mul_f32_e32 v3, v37, v2
	s_waitcnt lgkmcnt(0)
	s_nop 1
	v_mov_b32_dpp v4, v3 quad_perm:[1,0,3,2] row_mask:0xf bank_mask:0xf
	s_and_saveexec_b64 s[0:1], s[2:3]
	s_cbranch_execz .LBB0_1947
	v_add_co_u32_e32 v18, vcc, 0x3000, v70
	s_waitcnt lgkmcnt(0)
	v_cvt_pk_bf16_f32 v3, v3, v4
	s_nop 0
	v_addc_co_u32_e32 v19, vcc, 0, v71, vcc
	global_store_dword v[18:19], v3, off offset:64
.LBB0_1947:
	s_or_b64 exec, exec, s[0:1]
	v_mul_f32_e32 v3, v21, v2
	s_waitcnt lgkmcnt(0)
	s_nop 1
	v_mov_b32_dpp v4, v3 quad_perm:[1,0,3,2] row_mask:0xf bank_mask:0xf
	s_and_saveexec_b64 s[0:1], s[2:3]
	s_cbranch_execz .LBB0_1949
	v_add_co_u32_e32 v18, vcc, 0x3000, v70
	s_waitcnt lgkmcnt(0)
	v_cvt_pk_bf16_f32 v3, v3, v4
	s_nop 0
	v_addc_co_u32_e32 v19, vcc, 0, v71, vcc
	global_store_dword v[18:19], v3, off offset:128
.LBB0_1949:
	s_or_b64 exec, exec, s[0:1]
	v_mul_f32_e32 v2, v5, v2
	s_nop 1
	v_mov_b32_dpp v3, v2 quad_perm:[1,0,3,2] row_mask:0xf bank_mask:0xf
	s_and_saveexec_b64 s[0:1], s[2:3]
	s_cbranch_execz .LBB0_1951
	s_waitcnt lgkmcnt(0)
	v_cvt_pk_bf16_f32 v4, v2, v3
	v_add_co_u32_e32 v2, vcc, 0x3000, v70
	s_nop 1
	v_addc_co_u32_e32 v3, vcc, 0, v71, vcc
	global_store_dword v[2:3], v4, off offset:192
.LBB0_1951:
	s_or_b64 exec, exec, s[0:1]
	s_waitcnt lgkmcnt(0)
	ds_read_b128 v[2:5], v1 offset:32
	s_waitcnt lgkmcnt(0)
	v_rcp_f32_e32 v2, v2
	s_nop 0
	v_mul_f32_e32 v18, v54, v2
	s_nop 1
	v_mov_b32_dpp v19, v18 quad_perm:[1,0,3,2] row_mask:0xf bank_mask:0xf
	s_and_saveexec_b64 s[0:1], s[2:3]
	s_cbranch_execz .LBB0_1953
	s_waitcnt lgkmcnt(0)
	v_cvt_pk_bf16_f32 v20, v18, v19
	v_add_co_u32_e32 v18, vcc, 0x8000, v70
	s_nop 1
	v_addc_co_u32_e32 v19, vcc, 0, v71, vcc
	global_store_dword v[18:19], v20, off
.LBB0_1953:
	s_or_b64 exec, exec, s[0:1]
	v_mul_f32_e32 v18, v38, v2
	s_waitcnt lgkmcnt(0)
	s_nop 1
	v_mov_b32_dpp v19, v18 quad_perm:[1,0,3,2] row_mask:0xf bank_mask:0xf
	s_and_saveexec_b64 s[0:1], s[2:3]
	s_cbranch_execz .LBB0_1955
	s_waitcnt lgkmcnt(0)
	v_cvt_pk_bf16_f32 v20, v18, v19
	v_add_co_u32_e32 v18, vcc, 0x8000, v70
	s_nop 1
	v_addc_co_u32_e32 v19, vcc, 0, v71, vcc
	global_store_dword v[18:19], v20, off offset:64
.LBB0_1955:
	s_or_b64 exec, exec, s[0:1]
	v_mul_f32_e32 v18, v22, v2
	s_waitcnt lgkmcnt(0)
	s_nop 1
	v_mov_b32_dpp v19, v18 quad_perm:[1,0,3,2] row_mask:0xf bank_mask:0xf
	s_and_saveexec_b64 s[0:1], s[2:3]
	s_cbranch_execz .LBB0_1957
	s_waitcnt lgkmcnt(0)
	v_cvt_pk_bf16_f32 v20, v18, v19
	v_add_co_u32_e32 v18, vcc, 0x8000, v70
	s_nop 1
	v_addc_co_u32_e32 v19, vcc, 0, v71, vcc
	global_store_dword v[18:19], v20, off offset:128
.LBB0_1957:
	s_or_b64 exec, exec, s[0:1]
	v_mul_f32_e32 v2, v6, v2
	s_nop 1
	v_mov_b32_dpp v6, v2 quad_perm:[1,0,3,2] row_mask:0xf bank_mask:0xf
	s_and_saveexec_b64 s[0:1], s[2:3]
	s_cbranch_execz .LBB0_1959
	v_add_co_u32_e32 v18, vcc, 0x8000, v70
	s_waitcnt lgkmcnt(0)
	v_cvt_pk_bf16_f32 v2, v2, v6
	s_nop 0
	v_addc_co_u32_e32 v19, vcc, 0, v71, vcc
	global_store_dword v[18:19], v2, off offset:192
.LBB0_1959:
	s_or_b64 exec, exec, s[0:1]
	v_rcp_f32_e32 v2, v3
	s_nop 0
	v_mul_f32_e32 v3, v55, v2
	s_waitcnt lgkmcnt(0)
	s_nop 1
	v_mov_b32_dpp v6, v3 quad_perm:[1,0,3,2] row_mask:0xf bank_mask:0xf
	s_and_saveexec_b64 s[0:1], s[2:3]
	s_cbranch_execz .LBB0_1961
	v_add_co_u32_e32 v18, vcc, 0x9000, v70
	s_waitcnt lgkmcnt(0)
	v_cvt_pk_bf16_f32 v3, v3, v6
	s_nop 0
	v_addc_co_u32_e32 v19, vcc, 0, v71, vcc
	global_store_dword v[18:19], v3, off
.LBB0_1961:
	s_or_b64 exec, exec, s[0:1]
	v_mul_f32_e32 v3, v39, v2
	s_waitcnt lgkmcnt(0)
	s_nop 1
	v_mov_b32_dpp v6, v3 quad_perm:[1,0,3,2] row_mask:0xf bank_mask:0xf
	s_and_saveexec_b64 s[0:1], s[2:3]
	s_cbranch_execz .LBB0_1963
	v_add_co_u32_e32 v18, vcc, 0x9000, v70
	s_waitcnt lgkmcnt(0)
	v_cvt_pk_bf16_f32 v3, v3, v6
	s_nop 0
	v_addc_co_u32_e32 v19, vcc, 0, v71, vcc
	global_store_dword v[18:19], v3, off offset:64
.LBB0_1963:
	s_or_b64 exec, exec, s[0:1]
	v_mul_f32_e32 v3, v23, v2
	s_waitcnt lgkmcnt(0)
	s_nop 1
	v_mov_b32_dpp v6, v3 quad_perm:[1,0,3,2] row_mask:0xf bank_mask:0xf
	s_and_saveexec_b64 s[0:1], s[2:3]
	s_cbranch_execz .LBB0_1965
	v_add_co_u32_e32 v18, vcc, 0x9000, v70
	s_waitcnt lgkmcnt(0)
	v_cvt_pk_bf16_f32 v3, v3, v6
	s_nop 0
	v_addc_co_u32_e32 v19, vcc, 0, v71, vcc
	global_store_dword v[18:19], v3, off offset:128
.LBB0_1965:
	s_or_b64 exec, exec, s[0:1]
	v_mul_f32_e32 v2, v7, v2
	s_nop 1
	v_mov_b32_dpp v3, v2 quad_perm:[1,0,3,2] row_mask:0xf bank_mask:0xf
	s_and_saveexec_b64 s[0:1], s[2:3]
	s_cbranch_execz .LBB0_1967
	s_waitcnt lgkmcnt(0)
	v_cvt_pk_bf16_f32 v6, v2, v3
	v_add_co_u32_e32 v2, vcc, 0x9000, v70
	s_nop 1
	v_addc_co_u32_e32 v3, vcc, 0, v71, vcc
	global_store_dword v[2:3], v6, off offset:192
.LBB0_1967:
	s_or_b64 exec, exec, s[0:1]
	v_rcp_f32_e32 v2, v4
	s_waitcnt lgkmcnt(0)
	v_mul_f32_e32 v3, v56, v2
	s_nop 1
	v_mov_b32_dpp v4, v3 quad_perm:[1,0,3,2] row_mask:0xf bank_mask:0xf
	s_and_saveexec_b64 s[0:1], s[2:3]
	s_cbranch_execz .LBB0_1969
	v_add_co_u32_e32 v6, vcc, 0xa000, v70
	s_waitcnt lgkmcnt(0)
	v_cvt_pk_bf16_f32 v3, v3, v4
	s_nop 0
	v_addc_co_u32_e32 v7, vcc, 0, v71, vcc
	global_store_dword v[6:7], v3, off
.LBB0_1969:
	s_or_b64 exec, exec, s[0:1]
	v_mul_f32_e32 v3, v40, v2
	s_waitcnt lgkmcnt(0)
	s_nop 1
	v_mov_b32_dpp v4, v3 quad_perm:[1,0,3,2] row_mask:0xf bank_mask:0xf
	s_and_saveexec_b64 s[0:1], s[2:3]
	s_cbranch_execz .LBB0_1971
	v_add_co_u32_e32 v6, vcc, 0xa000, v70
	s_waitcnt lgkmcnt(0)
	v_cvt_pk_bf16_f32 v3, v3, v4
	s_nop 0
	v_addc_co_u32_e32 v7, vcc, 0, v71, vcc
	global_store_dword v[6:7], v3, off offset:64
.LBB0_1971:
	s_or_b64 exec, exec, s[0:1]
	v_mul_f32_e32 v3, v24, v2
	s_waitcnt lgkmcnt(0)
	s_nop 1
	v_mov_b32_dpp v4, v3 quad_perm:[1,0,3,2] row_mask:0xf bank_mask:0xf
	s_and_saveexec_b64 s[0:1], s[2:3]
	s_cbranch_execz .LBB0_1973
	v_add_co_u32_e32 v6, vcc, 0xa000, v70
	s_waitcnt lgkmcnt(0)
	v_cvt_pk_bf16_f32 v3, v3, v4
	s_nop 0
	v_addc_co_u32_e32 v7, vcc, 0, v71, vcc
	global_store_dword v[6:7], v3, off offset:128
.LBB0_1973:
	s_or_b64 exec, exec, s[0:1]
	v_mul_f32_e32 v2, v8, v2
	s_nop 1
	v_mov_b32_dpp v3, v2 quad_perm:[1,0,3,2] row_mask:0xf bank_mask:0xf
	s_and_saveexec_b64 s[0:1], s[2:3]
	s_cbranch_execz .LBB0_1975
	s_waitcnt lgkmcnt(0)
	v_cvt_pk_bf16_f32 v4, v2, v3
	v_add_co_u32_e32 v2, vcc, 0xa000, v70
	s_nop 1
	v_addc_co_u32_e32 v3, vcc, 0, v71, vcc
	global_store_dword v[2:3], v4, off offset:192
.LBB0_1975:
	s_or_b64 exec, exec, s[0:1]
	v_rcp_f32_e32 v2, v5
	s_waitcnt lgkmcnt(0)
	v_mul_f32_e32 v3, v57, v2
	s_nop 1
	v_mov_b32_dpp v4, v3 quad_perm:[1,0,3,2] row_mask:0xf bank_mask:0xf
	s_and_saveexec_b64 s[0:1], s[2:3]
	s_cbranch_execz .LBB0_1977
	s_waitcnt lgkmcnt(0)
	v_cvt_pk_bf16_f32 v3, v3, v4
	v_add_co_u32_e32 v4, vcc, 0xb000, v70
	s_nop 1
	v_addc_co_u32_e32 v5, vcc, 0, v71, vcc
	global_store_dword v[4:5], v3, off
.LBB0_1977:
	s_or_b64 exec, exec, s[0:1]
	v_mul_f32_e32 v3, v41, v2
	s_waitcnt lgkmcnt(0)
	s_nop 1
	v_mov_b32_dpp v4, v3 quad_perm:[1,0,3,2] row_mask:0xf bank_mask:0xf
	s_and_saveexec_b64 s[0:1], s[2:3]
	s_cbranch_execz .LBB0_1979
	s_waitcnt lgkmcnt(0)
	v_cvt_pk_bf16_f32 v3, v3, v4
	v_add_co_u32_e32 v4, vcc, 0xb000, v70
	s_nop 1
	v_addc_co_u32_e32 v5, vcc, 0, v71, vcc
	global_store_dword v[4:5], v3, off offset:64
.LBB0_1979:
	s_or_b64 exec, exec, s[0:1]
	v_mul_f32_e32 v3, v25, v2
	s_waitcnt lgkmcnt(0)
	s_nop 1
	v_mov_b32_dpp v4, v3 quad_perm:[1,0,3,2] row_mask:0xf bank_mask:0xf
	s_and_saveexec_b64 s[0:1], s[2:3]
	s_cbranch_execz .LBB0_1981
	s_waitcnt lgkmcnt(0)
	v_cvt_pk_bf16_f32 v3, v3, v4
	v_add_co_u32_e32 v4, vcc, 0xb000, v70
	s_nop 1
	v_addc_co_u32_e32 v5, vcc, 0, v71, vcc
	global_store_dword v[4:5], v3, off offset:128
.LBB0_1981:
	s_or_b64 exec, exec, s[0:1]
	v_mul_f32_e32 v2, v9, v2
	s_nop 1
	v_mov_b32_dpp v3, v2 quad_perm:[1,0,3,2] row_mask:0xf bank_mask:0xf
	s_and_saveexec_b64 s[0:1], s[2:3]
	s_cbranch_execz .LBB0_1983
	s_waitcnt lgkmcnt(0)
	v_cvt_pk_bf16_f32 v4, v2, v3
	v_add_co_u32_e32 v2, vcc, 0xb000, v70
	s_nop 1
	v_addc_co_u32_e32 v3, vcc, 0, v71, vcc
	global_store_dword v[2:3], v4, off offset:192
.LBB0_1983:
	s_or_b64 exec, exec, s[0:1]
	s_waitcnt lgkmcnt(0)
	ds_read_b128 v[2:5], v1 offset:64
	s_waitcnt lgkmcnt(0)
	v_rcp_f32_e32 v2, v2
	s_nop 0
	v_mul_f32_e32 v6, v58, v2
	s_nop 1
	v_mov_b32_dpp v7, v6 quad_perm:[1,0,3,2] row_mask:0xf bank_mask:0xf
	s_and_saveexec_b64 s[0:1], s[2:3]
	s_cbranch_execz .LBB0_1985
	s_waitcnt lgkmcnt(0)
	v_cvt_pk_bf16_f32 v8, v6, v7
	v_add_co_u32_e32 v6, vcc, 0x10000, v70
	s_nop 1
	v_addc_co_u32_e32 v7, vcc, 0, v71, vcc
	global_store_dword v[6:7], v8, off
.LBB0_1985:
	s_or_b64 exec, exec, s[0:1]
	v_mul_f32_e32 v6, v42, v2
	s_waitcnt lgkmcnt(0)
	s_nop 1
	v_mov_b32_dpp v7, v6 quad_perm:[1,0,3,2] row_mask:0xf bank_mask:0xf
	s_and_saveexec_b64 s[0:1], s[2:3]
	s_cbranch_execz .LBB0_1987
	s_waitcnt lgkmcnt(0)
	v_cvt_pk_bf16_f32 v8, v6, v7
	v_add_co_u32_e32 v6, vcc, 0x10000, v70
	s_nop 1
	v_addc_co_u32_e32 v7, vcc, 0, v71, vcc
	global_store_dword v[6:7], v8, off offset:64
.LBB0_1987:
	s_or_b64 exec, exec, s[0:1]
	v_mul_f32_e32 v6, v26, v2
	s_waitcnt lgkmcnt(0)
	s_nop 1
	v_mov_b32_dpp v7, v6 quad_perm:[1,0,3,2] row_mask:0xf bank_mask:0xf
	s_and_saveexec_b64 s[0:1], s[2:3]
	s_cbranch_execz .LBB0_1989
	s_waitcnt lgkmcnt(0)
	v_cvt_pk_bf16_f32 v8, v6, v7
	v_add_co_u32_e32 v6, vcc, 0x10000, v70
	s_nop 1
	v_addc_co_u32_e32 v7, vcc, 0, v71, vcc
	global_store_dword v[6:7], v8, off offset:128
.LBB0_1989:
	s_or_b64 exec, exec, s[0:1]
	v_mul_f32_e32 v2, v10, v2
	s_nop 1
	v_mov_b32_dpp v6, v2 quad_perm:[1,0,3,2] row_mask:0xf bank_mask:0xf
	s_and_saveexec_b64 s[0:1], s[2:3]
	s_cbranch_execz .LBB0_1991
	s_waitcnt lgkmcnt(0)
	v_cvt_pk_bf16_f32 v2, v2, v6
	v_add_co_u32_e32 v6, vcc, 0x10000, v70
	s_nop 1
	v_addc_co_u32_e32 v7, vcc, 0, v71, vcc
	global_store_dword v[6:7], v2, off offset:192
.LBB0_1991:
	s_or_b64 exec, exec, s[0:1]
	v_rcp_f32_e32 v2, v3
	s_nop 0
	v_mul_f32_e32 v3, v59, v2
	s_waitcnt lgkmcnt(0)
	s_nop 1
	v_mov_b32_dpp v6, v3 quad_perm:[1,0,3,2] row_mask:0xf bank_mask:0xf
	s_and_saveexec_b64 s[0:1], s[2:3]
	s_cbranch_execz .LBB0_1993
	s_waitcnt lgkmcnt(0)
	v_cvt_pk_bf16_f32 v3, v3, v6
	v_add_co_u32_e32 v6, vcc, 0x11000, v70
	s_nop 1
	v_addc_co_u32_e32 v7, vcc, 0, v71, vcc
	global_store_dword v[6:7], v3, off
.LBB0_1993:
	s_or_b64 exec, exec, s[0:1]
	v_mul_f32_e32 v3, v43, v2
	s_waitcnt lgkmcnt(0)
	s_nop 1
	v_mov_b32_dpp v6, v3 quad_perm:[1,0,3,2] row_mask:0xf bank_mask:0xf
	s_and_saveexec_b64 s[0:1], s[2:3]
	s_cbranch_execz .LBB0_1995
	s_waitcnt lgkmcnt(0)
	v_cvt_pk_bf16_f32 v3, v3, v6
	v_add_co_u32_e32 v6, vcc, 0x11000, v70
	s_nop 1
	v_addc_co_u32_e32 v7, vcc, 0, v71, vcc
	global_store_dword v[6:7], v3, off offset:64
.LBB0_1995:
	s_or_b64 exec, exec, s[0:1]
	v_mul_f32_e32 v3, v27, v2
	s_waitcnt lgkmcnt(0)
	s_nop 1
	v_mov_b32_dpp v6, v3 quad_perm:[1,0,3,2] row_mask:0xf bank_mask:0xf
	s_and_saveexec_b64 s[0:1], s[2:3]
	s_cbranch_execz .LBB0_1997
	s_waitcnt lgkmcnt(0)
	v_cvt_pk_bf16_f32 v3, v3, v6
	v_add_co_u32_e32 v6, vcc, 0x11000, v70
	s_nop 1
	v_addc_co_u32_e32 v7, vcc, 0, v71, vcc
	global_store_dword v[6:7], v3, off offset:128
.LBB0_1997:
	s_or_b64 exec, exec, s[0:1]
	v_mul_f32_e32 v2, v11, v2
	s_nop 1
	v_mov_b32_dpp v3, v2 quad_perm:[1,0,3,2] row_mask:0xf bank_mask:0xf
	s_and_saveexec_b64 s[0:1], s[2:3]
	s_cbranch_execz .LBB0_1999
	s_waitcnt lgkmcnt(0)
	v_cvt_pk_bf16_f32 v6, v2, v3
	v_add_co_u32_e32 v2, vcc, 0x11000, v70
	s_nop 1
	v_addc_co_u32_e32 v3, vcc, 0, v71, vcc
	global_store_dword v[2:3], v6, off offset:192
.LBB0_1999:
	s_or_b64 exec, exec, s[0:1]
	v_rcp_f32_e32 v2, v4
	s_waitcnt lgkmcnt(0)
	v_mul_f32_e32 v3, v60, v2
	s_nop 1
	v_mov_b32_dpp v4, v3 quad_perm:[1,0,3,2] row_mask:0xf bank_mask:0xf
	s_and_saveexec_b64 s[0:1], s[2:3]
	s_cbranch_execz .LBB0_2001
	v_add_co_u32_e32 v6, vcc, 0x12000, v70
	s_waitcnt lgkmcnt(0)
	v_cvt_pk_bf16_f32 v3, v3, v4
	s_nop 0
	v_addc_co_u32_e32 v7, vcc, 0, v71, vcc
	global_store_dword v[6:7], v3, off
.LBB0_2001:
	s_or_b64 exec, exec, s[0:1]
	v_mul_f32_e32 v3, v44, v2
	s_waitcnt lgkmcnt(0)
	s_nop 1
	v_mov_b32_dpp v4, v3 quad_perm:[1,0,3,2] row_mask:0xf bank_mask:0xf
	s_and_saveexec_b64 s[0:1], s[2:3]
	s_cbranch_execz .LBB0_2003
	v_add_co_u32_e32 v6, vcc, 0x12000, v70
	s_waitcnt lgkmcnt(0)
	v_cvt_pk_bf16_f32 v3, v3, v4
	s_nop 0
	v_addc_co_u32_e32 v7, vcc, 0, v71, vcc
	global_store_dword v[6:7], v3, off offset:64
.LBB0_2003:
	s_or_b64 exec, exec, s[0:1]
	v_mul_f32_e32 v3, v28, v2
	s_waitcnt lgkmcnt(0)
	s_nop 1
	v_mov_b32_dpp v4, v3 quad_perm:[1,0,3,2] row_mask:0xf bank_mask:0xf
	s_and_saveexec_b64 s[0:1], s[2:3]
	s_cbranch_execz .LBB0_2005
	v_add_co_u32_e32 v6, vcc, 0x12000, v70
	s_waitcnt lgkmcnt(0)
	v_cvt_pk_bf16_f32 v3, v3, v4
	s_nop 0
	v_addc_co_u32_e32 v7, vcc, 0, v71, vcc
	global_store_dword v[6:7], v3, off offset:128
.LBB0_2005:
	s_or_b64 exec, exec, s[0:1]
	v_mul_f32_e32 v2, v12, v2
	s_nop 1
	v_mov_b32_dpp v3, v2 quad_perm:[1,0,3,2] row_mask:0xf bank_mask:0xf
	s_and_saveexec_b64 s[0:1], s[2:3]
	s_cbranch_execz .LBB0_2007
	s_waitcnt lgkmcnt(0)
	v_cvt_pk_bf16_f32 v4, v2, v3
	v_add_co_u32_e32 v2, vcc, 0x12000, v70
	s_nop 1
	v_addc_co_u32_e32 v3, vcc, 0, v71, vcc
	global_store_dword v[2:3], v4, off offset:192
.LBB0_2007:
	s_or_b64 exec, exec, s[0:1]
	v_rcp_f32_e32 v2, v5
	s_waitcnt lgkmcnt(0)
	v_mul_f32_e32 v3, v61, v2
	s_nop 1
	v_mov_b32_dpp v4, v3 quad_perm:[1,0,3,2] row_mask:0xf bank_mask:0xf
	s_and_saveexec_b64 s[0:1], s[2:3]
	s_cbranch_execz .LBB0_2009
	s_waitcnt lgkmcnt(0)
	v_cvt_pk_bf16_f32 v3, v3, v4
	v_add_co_u32_e32 v4, vcc, 0x13000, v70
	s_nop 1
	v_addc_co_u32_e32 v5, vcc, 0, v71, vcc
	global_store_dword v[4:5], v3, off
.LBB0_2009:
	s_or_b64 exec, exec, s[0:1]
	v_mul_f32_e32 v3, v45, v2
	s_waitcnt lgkmcnt(0)
	s_nop 1
	v_mov_b32_dpp v4, v3 quad_perm:[1,0,3,2] row_mask:0xf bank_mask:0xf
	s_and_saveexec_b64 s[0:1], s[2:3]
	s_cbranch_execz .LBB0_2011
	s_waitcnt lgkmcnt(0)
	v_cvt_pk_bf16_f32 v3, v3, v4
	v_add_co_u32_e32 v4, vcc, 0x13000, v70
	s_nop 1
	v_addc_co_u32_e32 v5, vcc, 0, v71, vcc
	global_store_dword v[4:5], v3, off offset:64
.LBB0_2011:
	s_or_b64 exec, exec, s[0:1]
	v_mul_f32_e32 v3, v29, v2
	s_waitcnt lgkmcnt(0)
	s_nop 1
	v_mov_b32_dpp v4, v3 quad_perm:[1,0,3,2] row_mask:0xf bank_mask:0xf
	s_and_saveexec_b64 s[0:1], s[2:3]
	s_cbranch_execz .LBB0_2013
	s_waitcnt lgkmcnt(0)
	v_cvt_pk_bf16_f32 v3, v3, v4
	v_add_co_u32_e32 v4, vcc, 0x13000, v70
	s_nop 1
	v_addc_co_u32_e32 v5, vcc, 0, v71, vcc
	global_store_dword v[4:5], v3, off offset:128
.LBB0_2013:
	s_or_b64 exec, exec, s[0:1]
	v_mul_f32_e32 v2, v13, v2
	s_nop 1
	v_mov_b32_dpp v3, v2 quad_perm:[1,0,3,2] row_mask:0xf bank_mask:0xf
	s_and_saveexec_b64 s[0:1], s[2:3]
	s_cbranch_execz .LBB0_2015
	s_waitcnt lgkmcnt(0)
	v_cvt_pk_bf16_f32 v4, v2, v3
	v_add_co_u32_e32 v2, vcc, 0x13000, v70
	s_nop 1
	v_addc_co_u32_e32 v3, vcc, 0, v71, vcc
	global_store_dword v[2:3], v4, off offset:192
.LBB0_2015:
	s_or_b64 exec, exec, s[0:1]
	s_waitcnt lgkmcnt(0)
	ds_read_b128 v[2:5], v1 offset:96
	s_waitcnt lgkmcnt(0)
	v_rcp_f32_e32 v1, v2
	s_nop 0
	v_mul_f32_e32 v2, v62, v1
	s_nop 1
	v_mov_b32_dpp v6, v2 quad_perm:[1,0,3,2] row_mask:0xf bank_mask:0xf
	s_and_saveexec_b64 s[0:1], s[2:3]
	s_cbranch_execz .LBB0_2017
	s_waitcnt lgkmcnt(0)
	v_cvt_pk_bf16_f32 v2, v2, v6
	v_add_co_u32_e32 v6, vcc, 0x18000, v70
	s_nop 1
	v_addc_co_u32_e32 v7, vcc, 0, v71, vcc
	global_store_dword v[6:7], v2, off
.LBB0_2017:
	s_or_b64 exec, exec, s[0:1]
	v_mul_f32_e32 v2, v46, v1
	s_waitcnt lgkmcnt(0)
	s_nop 1
	v_mov_b32_dpp v6, v2 quad_perm:[1,0,3,2] row_mask:0xf bank_mask:0xf
	s_and_saveexec_b64 s[0:1], s[2:3]
	s_cbranch_execz .LBB0_2019
	s_waitcnt lgkmcnt(0)
	v_cvt_pk_bf16_f32 v2, v2, v6
	v_add_co_u32_e32 v6, vcc, 0x18000, v70
	s_nop 1
	v_addc_co_u32_e32 v7, vcc, 0, v71, vcc
	global_store_dword v[6:7], v2, off offset:64
.LBB0_2019:
	s_or_b64 exec, exec, s[0:1]
	v_mul_f32_e32 v2, v30, v1
	s_waitcnt lgkmcnt(0)
	s_nop 1
	v_mov_b32_dpp v6, v2 quad_perm:[1,0,3,2] row_mask:0xf bank_mask:0xf
	s_and_saveexec_b64 s[0:1], s[2:3]
	s_cbranch_execz .LBB0_2021
	s_waitcnt lgkmcnt(0)
	v_cvt_pk_bf16_f32 v2, v2, v6
	v_add_co_u32_e32 v6, vcc, 0x18000, v70
	s_nop 1
	v_addc_co_u32_e32 v7, vcc, 0, v71, vcc
	global_store_dword v[6:7], v2, off offset:128
.LBB0_2021:
	s_or_b64 exec, exec, s[0:1]
	v_mul_f32_e32 v1, v14, v1
	s_nop 1
	v_mov_b32_dpp v2, v1 quad_perm:[1,0,3,2] row_mask:0xf bank_mask:0xf
	s_and_saveexec_b64 s[0:1], s[2:3]
	s_cbranch_execz .LBB0_2023
	s_waitcnt lgkmcnt(1)
	v_add_co_u32_e32 v6, vcc, 0x18000, v70
	s_waitcnt lgkmcnt(0)
	v_cvt_pk_bf16_f32 v1, v1, v2
	s_nop 0
	v_addc_co_u32_e32 v7, vcc, 0, v71, vcc
	global_store_dword v[6:7], v1, off offset:192
.LBB0_2023:
	s_or_b64 exec, exec, s[0:1]
	v_rcp_f32_e32 v1, v3
	s_waitcnt lgkmcnt(0)
	v_mul_f32_e32 v2, v63, v1
	s_nop 1
	v_mov_b32_dpp v3, v2 quad_perm:[1,0,3,2] row_mask:0xf bank_mask:0xf
	s_and_saveexec_b64 s[0:1], s[2:3]
	s_cbranch_execz .LBB0_2025
	s_waitcnt lgkmcnt(0)
	v_cvt_pk_bf16_f32 v6, v2, v3
	v_add_co_u32_e32 v2, vcc, 0x19000, v70
	s_nop 1
	v_addc_co_u32_e32 v3, vcc, 0, v71, vcc
	global_store_dword v[2:3], v6, off
.LBB0_2025:
	s_or_b64 exec, exec, s[0:1]
	v_mul_f32_e32 v2, v47, v1
	s_waitcnt lgkmcnt(0)
	s_nop 1
	v_mov_b32_dpp v3, v2 quad_perm:[1,0,3,2] row_mask:0xf bank_mask:0xf
	s_and_saveexec_b64 s[0:1], s[2:3]
	s_cbranch_execz .LBB0_2027
	s_waitcnt lgkmcnt(0)
	v_cvt_pk_bf16_f32 v6, v2, v3
	v_add_co_u32_e32 v2, vcc, 0x19000, v70
	s_nop 1
	v_addc_co_u32_e32 v3, vcc, 0, v71, vcc
	global_store_dword v[2:3], v6, off offset:64
.LBB0_2027:
	s_or_b64 exec, exec, s[0:1]
	v_mul_f32_e32 v2, v31, v1
	s_waitcnt lgkmcnt(0)
	s_nop 1
	v_mov_b32_dpp v3, v2 quad_perm:[1,0,3,2] row_mask:0xf bank_mask:0xf
	s_and_saveexec_b64 s[0:1], s[2:3]
	s_cbranch_execz .LBB0_2029
	s_waitcnt lgkmcnt(0)
	v_cvt_pk_bf16_f32 v6, v2, v3
	v_add_co_u32_e32 v2, vcc, 0x19000, v70
	s_nop 1
	v_addc_co_u32_e32 v3, vcc, 0, v71, vcc
	global_store_dword v[2:3], v6, off offset:128
.LBB0_2029:
	s_or_b64 exec, exec, s[0:1]
	v_mul_f32_e32 v1, v15, v1
	s_nop 1
	v_mov_b32_dpp v2, v1 quad_perm:[1,0,3,2] row_mask:0xf bank_mask:0xf
	s_and_saveexec_b64 s[0:1], s[2:3]
	s_cbranch_execz .LBB0_2031
	s_waitcnt lgkmcnt(0)
	v_cvt_pk_bf16_f32 v1, v1, v2
	v_add_co_u32_e32 v2, vcc, 0x19000, v70
	s_nop 1
	v_addc_co_u32_e32 v3, vcc, 0, v71, vcc
	global_store_dword v[2:3], v1, off offset:192
.LBB0_2031:
	s_or_b64 exec, exec, s[0:1]
	v_rcp_f32_e32 v1, v4
	s_waitcnt lgkmcnt(0)
	v_mul_f32_e32 v2, v64, v1
	s_nop 1
	v_mov_b32_dpp v3, v2 quad_perm:[1,0,3,2] row_mask:0xf bank_mask:0xf
	s_and_saveexec_b64 s[0:1], s[2:3]
	s_cbranch_execz .LBB0_2033
	s_waitcnt lgkmcnt(0)
	v_cvt_pk_bf16_f32 v4, v2, v3
	v_add_co_u32_e32 v2, vcc, 0x1a000, v70
	s_nop 1
	v_addc_co_u32_e32 v3, vcc, 0, v71, vcc
	global_store_dword v[2:3], v4, off
.LBB0_2033:
	s_or_b64 exec, exec, s[0:1]
	v_mul_f32_e32 v2, v48, v1
	s_waitcnt lgkmcnt(0)
	s_nop 1
	v_mov_b32_dpp v3, v2 quad_perm:[1,0,3,2] row_mask:0xf bank_mask:0xf
	s_and_saveexec_b64 s[0:1], s[2:3]
	s_cbranch_execz .LBB0_2035
	s_waitcnt lgkmcnt(0)
	v_cvt_pk_bf16_f32 v4, v2, v3
	v_add_co_u32_e32 v2, vcc, 0x1a000, v70
	s_nop 1
	v_addc_co_u32_e32 v3, vcc, 0, v71, vcc
	global_store_dword v[2:3], v4, off offset:64
.LBB0_2035:
	s_or_b64 exec, exec, s[0:1]
	v_mul_f32_e32 v2, v32, v1
	s_waitcnt lgkmcnt(0)
	s_nop 1
	v_mov_b32_dpp v3, v2 quad_perm:[1,0,3,2] row_mask:0xf bank_mask:0xf
	s_and_saveexec_b64 s[0:1], s[2:3]
	s_cbranch_execz .LBB0_2037
	s_waitcnt lgkmcnt(0)
	v_cvt_pk_bf16_f32 v4, v2, v3
	v_add_co_u32_e32 v2, vcc, 0x1a000, v70
	s_nop 1
	v_addc_co_u32_e32 v3, vcc, 0, v71, vcc
	global_store_dword v[2:3], v4, off offset:128
.LBB0_2037:
	s_or_b64 exec, exec, s[0:1]
	v_mul_f32_e32 v1, v16, v1
	s_nop 1
	v_mov_b32_dpp v2, v1 quad_perm:[1,0,3,2] row_mask:0xf bank_mask:0xf
	s_and_saveexec_b64 s[0:1], s[2:3]
	s_cbranch_execz .LBB0_2039
	s_waitcnt lgkmcnt(0)
	v_cvt_pk_bf16_f32 v1, v1, v2
	v_add_co_u32_e32 v2, vcc, 0x1a000, v70
	s_nop 1
	v_addc_co_u32_e32 v3, vcc, 0, v71, vcc
	global_store_dword v[2:3], v1, off offset:192
.LBB0_2039:
	s_or_b64 exec, exec, s[0:1]
	v_rcp_f32_e32 v1, v5
	s_waitcnt lgkmcnt(0)
	v_mul_f32_e32 v2, v65, v1
	s_nop 1
	v_mov_b32_dpp v3, v2 quad_perm:[1,0,3,2] row_mask:0xf bank_mask:0xf
	s_and_saveexec_b64 s[0:1], s[2:3]
	s_cbranch_execz .LBB0_2041
	s_waitcnt lgkmcnt(0)
	v_cvt_pk_bf16_f32 v4, v2, v3
	v_add_co_u32_e32 v2, vcc, 0x1b000, v70
	s_nop 1
	v_addc_co_u32_e32 v3, vcc, 0, v71, vcc
	global_store_dword v[2:3], v4, off
.LBB0_2041:
	s_or_b64 exec, exec, s[0:1]
	v_mul_f32_e32 v2, v49, v1
	s_waitcnt lgkmcnt(0)
	s_nop 1
	v_mov_b32_dpp v3, v2 quad_perm:[1,0,3,2] row_mask:0xf bank_mask:0xf
	s_and_saveexec_b64 s[0:1], s[2:3]
	s_cbranch_execz .LBB0_2043
	s_waitcnt lgkmcnt(0)
	v_cvt_pk_bf16_f32 v4, v2, v3
	v_add_co_u32_e32 v2, vcc, 0x1b000, v70
	s_nop 1
	v_addc_co_u32_e32 v3, vcc, 0, v71, vcc
	global_store_dword v[2:3], v4, off offset:64
.LBB0_2043:
	s_or_b64 exec, exec, s[0:1]
	v_mul_f32_e32 v2, v33, v1
	s_waitcnt lgkmcnt(0)
	s_nop 1
	v_mov_b32_dpp v3, v2 quad_perm:[1,0,3,2] row_mask:0xf bank_mask:0xf
	s_and_saveexec_b64 s[0:1], s[2:3]
	s_cbranch_execz .LBB0_2045
	s_waitcnt lgkmcnt(0)
	v_cvt_pk_bf16_f32 v4, v2, v3
	v_add_co_u32_e32 v2, vcc, 0x1b000, v70
	s_nop 1
	v_addc_co_u32_e32 v3, vcc, 0, v71, vcc
	global_store_dword v[2:3], v4, off offset:128
.LBB0_2045:
	s_or_b64 exec, exec, s[0:1]
	v_mul_f32_e32 v1, v17, v1
	s_nop 1
	v_mov_b32_dpp v2, v1 quad_perm:[1,0,3,2] row_mask:0xf bank_mask:0xf
	s_and_saveexec_b64 s[0:1], s[2:3]
	s_cbranch_execz .LBB0_2047
	s_waitcnt lgkmcnt(0)
	v_cvt_pk_bf16_f32 v1, v1, v2
	v_add_co_u32_e32 v2, vcc, 0x1b000, v70
	s_nop 1
	v_addc_co_u32_e32 v3, vcc, 0, v71, vcc
	global_store_dword v[2:3], v1, off offset:192

.LBB0_2073:
	s_and_saveexec_b64 s[0:1], s[2:3]
	ds_write_b32 v176, v189
	s_or_b64 exec, exec, s[0:1]
	s_waitcnt lgkmcnt(0)
	v_add_u32_e32 v1, s77, v164
	ds_read_b128 v[66:69], v1
	s_ashr_i32 s77, s76, 31
	s_lshl_b64 s[0:1], s[76:77], 12
	s_add_u32 s2, s81, s0
	s_addc_u32 s3, s80, s1
	s_waitcnt lgkmcnt(0)
	v_rcp_f32_e32 v66, v66
	v_and_b32_e32 v70, 1, v172
	v_lshlrev_b32_e32 v86, 1, v171
	v_cmp_eq_u32_e64 s[0:1], 0, v70
	v_mul_f32_e32 v50, v50, v66
	s_nop 1
	v_mov_b32_dpp v72, v50 quad_perm:[1,0,3,2] row_mask:0xf bank_mask:0xf
	v_lshl_add_u64 v[70:71], s[2:3], 0, v[86:87]
	v_lshlrev_b32_e32 v86, 14, v170
	v_lshl_add_u64 v[70:71], v[70:71], 0, v[86:87]
	s_and_saveexec_b64 s[2:3], s[0:1]
	s_cbranch_execz .LBB0_2077
	s_waitcnt lgkmcnt(0)
	v_cvt_pk_bf16_f32 v50, v50, v72
	global_store_dword v[70:71], v50, off

.LBB0_2107:
	s_or_b64 exec, exec, s[2:3]
	s_waitcnt lgkmcnt(0)
	ds_read_b128 v[2:5], v1 offset:32
	s_waitcnt lgkmcnt(0)
	v_rcp_f32_e32 v2, v2
	s_nop 0
	v_mul_f32_e32 v18, v54, v2
	s_nop 1
	v_mov_b32_dpp v19, v18 quad_perm:[1,0,3,2] row_mask:0xf bank_mask:0xf
	s_and_saveexec_b64 s[2:3], s[0:1]
	s_cbranch_execz .LBB0_2109
	s_waitcnt lgkmcnt(0)
	v_cvt_pk_bf16_f32 v20, v18, v19
	v_add_co_u32_e32 v18, vcc, 0x8000, v70
	s_nop 1
	v_addc_co_u32_e32 v19, vcc, 0, v71, vcc
	global_store_dword v[18:19], v20, off

.LBB0_2139:
	s_or_b64 exec, exec, s[2:3]
	s_waitcnt lgkmcnt(0)
	ds_read_b128 v[2:5], v1 offset:64
	s_waitcnt lgkmcnt(0)
	v_rcp_f32_e32 v2, v2
	s_nop 0
	v_mul_f32_e32 v6, v58, v2
	s_nop 1
	v_mov_b32_dpp v7, v6 quad_perm:[1,0,3,2] row_mask:0xf bank_mask:0xf
	s_and_saveexec_b64 s[2:3], s[0:1]
	s_cbranch_execz .LBB0_2141
	s_waitcnt lgkmcnt(0)
	v_cvt_pk_bf16_f32 v8, v6, v7
	v_add_co_u32_e32 v6, vcc, 0x10000, v70
	s_nop 1
	v_addc_co_u32_e32 v7, vcc, 0, v71, vcc
	global_store_dword v[6:7], v8, off

.LBB0_2171:
	s_or_b64 exec, exec, s[2:3]
	s_waitcnt lgkmcnt(0)
	ds_read_b128 v[2:5], v1 offset:96
	s_waitcnt lgkmcnt(0)
	v_rcp_f32_e32 v1, v2
	s_nop 0
	v_mul_f32_e32 v2, v62, v1
	s_nop 1
	v_mov_b32_dpp v6, v2 quad_perm:[1,0,3,2] row_mask:0xf bank_mask:0xf
	s_and_saveexec_b64 s[2:3], s[0:1]
	s_cbranch_execz .LBB0_2173
	s_waitcnt lgkmcnt(0)
	v_cvt_pk_bf16_f32 v2, v2, v6
	v_add_co_u32_e32 v6, vcc, 0x18000, v70
	s_nop 1
	v_addc_co_u32_e32 v7, vcc, 0, v71, vcc
	global_store_dword v[6:7], v2, off
.LBB0_2173:
	s_or_b64 exec, exec, s[2:3]
	v_mul_f32_e32 v2, v46, v1
	s_waitcnt lgkmcnt(0)
	s_nop 1
	v_mov_b32_dpp v6, v2 quad_perm:[1,0,3,2] row_mask:0xf bank_mask:0xf
	s_and_saveexec_b64 s[2:3], s[0:1]
	s_cbranch_execz .LBB0_2175
	s_waitcnt lgkmcnt(0)
	v_cvt_pk_bf16_f32 v2, v2, v6
	v_add_co_u32_e32 v6, vcc, 0x18000, v70
	s_nop 1
	v_addc_co_u32_e32 v7, vcc, 0, v71, vcc
	global_store_dword v[6:7], v2, off offset:64
.LBB0_2175:
	s_or_b64 exec, exec, s[2:3]
	v_mul_f32_e32 v2, v30, v1
	s_waitcnt lgkmcnt(0)
	s_nop 1
	v_mov_b32_dpp v6, v2 quad_perm:[1,0,3,2] row_mask:0xf bank_mask:0xf
	s_and_saveexec_b64 s[2:3], s[0:1]
	s_cbranch_execz .LBB0_2177
	s_waitcnt lgkmcnt(0)
	v_cvt_pk_bf16_f32 v2, v2, v6
	v_add_co_u32_e32 v6, vcc, 0x18000, v70
	s_nop 1
	v_addc_co_u32_e32 v7, vcc, 0, v71, vcc
	global_store_dword v[6:7], v2, off offset:128
.LBB0_2177:
	s_or_b64 exec, exec, s[2:3]
	v_mul_f32_e32 v1, v14, v1
	s_nop 1
	v_mov_b32_dpp v2, v1 quad_perm:[1,0,3,2] row_mask:0xf bank_mask:0xf
	s_and_saveexec_b64 s[2:3], s[0:1]
	s_cbranch_execz .LBB0_2179
	s_waitcnt lgkmcnt(1)
	v_add_co_u32_e32 v6, vcc, 0x18000, v70
	s_waitcnt lgkmcnt(0)
	v_cvt_pk_bf16_f32 v1, v1, v2
	s_nop 0
	v_addc_co_u32_e32 v7, vcc, 0, v71, vcc
	global_store_dword v[6:7], v1, off offset:192
.LBB0_2179:
	s_or_b64 exec, exec, s[2:3]
	v_rcp_f32_e32 v1, v3
	s_waitcnt lgkmcnt(0)
	v_mul_f32_e32 v2, v63, v1
	s_nop 1
	v_mov_b32_dpp v3, v2 quad_perm:[1,0,3,2] row_mask:0xf bank_mask:0xf
	s_and_saveexec_b64 s[2:3], s[0:1]
	s_cbranch_execz .LBB0_2181
	s_waitcnt lgkmcnt(0)
	v_cvt_pk_bf16_f32 v6, v2, v3
	v_add_co_u32_e32 v2, vcc, 0x19000, v70
	s_nop 1
	v_addc_co_u32_e32 v3, vcc, 0, v71, vcc
	global_store_dword v[2:3], v6, off
.LBB0_2181:
	s_or_b64 exec, exec, s[2:3]
	v_mul_f32_e32 v2, v47, v1
	s_waitcnt lgkmcnt(0)
	s_nop 1
	v_mov_b32_dpp v3, v2 quad_perm:[1,0,3,2] row_mask:0xf bank_mask:0xf
	s_and_saveexec_b64 s[2:3], s[0:1]
	s_cbranch_execz .LBB0_2183
	s_waitcnt lgkmcnt(0)
	v_cvt_pk_bf16_f32 v6, v2, v3
	v_add_co_u32_e32 v2, vcc, 0x19000, v70
	s_nop 1
	v_addc_co_u32_e32 v3, vcc, 0, v71, vcc
	global_store_dword v[2:3], v6, off offset:64
.LBB0_2183:
	s_or_b64 exec, exec, s[2:3]
	v_mul_f32_e32 v2, v31, v1
	s_waitcnt lgkmcnt(0)
	s_nop 1
	v_mov_b32_dpp v3, v2 quad_perm:[1,0,3,2] row_mask:0xf bank_mask:0xf
	s_and_saveexec_b64 s[2:3], s[0:1]
	s_cbranch_execz .LBB0_2185
	s_waitcnt lgkmcnt(0)
	v_cvt_pk_bf16_f32 v6, v2, v3
	v_add_co_u32_e32 v2, vcc, 0x19000, v70
	s_nop 1
	v_addc_co_u32_e32 v3, vcc, 0, v71, vcc
	global_store_dword v[2:3], v6, off offset:128
.LBB0_2185:
	s_or_b64 exec, exec, s[2:3]
	v_mul_f32_e32 v1, v15, v1
	s_nop 1
	v_mov_b32_dpp v2, v1 quad_perm:[1,0,3,2] row_mask:0xf bank_mask:0xf
	s_and_saveexec_b64 s[2:3], s[0:1]
	s_cbranch_execz .LBB0_2187
	s_waitcnt lgkmcnt(0)
	v_cvt_pk_bf16_f32 v1, v1, v2
	v_add_co_u32_e32 v2, vcc, 0x19000, v70
	s_nop 1
	v_addc_co_u32_e32 v3, vcc, 0, v71, vcc
	global_store_dword v[2:3], v1, off offset:192
.LBB0_2187:
	s_or_b64 exec, exec, s[2:3]
	v_rcp_f32_e32 v1, v4
	s_waitcnt lgkmcnt(0)
	v_mul_f32_e32 v2, v64, v1
	s_nop 1
	v_mov_b32_dpp v3, v2 quad_perm:[1,0,3,2] row_mask:0xf bank_mask:0xf
	s_and_saveexec_b64 s[2:3], s[0:1]
	s_cbranch_execz .LBB0_2189
	s_waitcnt lgkmcnt(0)
	v_cvt_pk_bf16_f32 v4, v2, v3
	v_add_co_u32_e32 v2, vcc, 0x1a000, v70
	s_nop 1
	v_addc_co_u32_e32 v3, vcc, 0, v71, vcc
	global_store_dword v[2:3], v4, off
.LBB0_2189:
	s_or_b64 exec, exec, s[2:3]
	v_mul_f32_e32 v2, v48, v1
	s_waitcnt lgkmcnt(0)
	s_nop 1
	v_mov_b32_dpp v3, v2 quad_perm:[1,0,3,2] row_mask:0xf bank_mask:0xf
	s_and_saveexec_b64 s[2:3], s[0:1]
	s_cbranch_execz .LBB0_2191
	s_waitcnt lgkmcnt(0)
	v_cvt_pk_bf16_f32 v4, v2, v3
	v_add_co_u32_e32 v2, vcc, 0x1a000, v70
	s_nop 1
	v_addc_co_u32_e32 v3, vcc, 0, v71, vcc
	global_store_dword v[2:3], v4, off offset:64
.LBB0_2191:
	s_or_b64 exec, exec, s[2:3]
	v_mul_f32_e32 v2, v32, v1
	s_waitcnt lgkmcnt(0)
	s_nop 1
	v_mov_b32_dpp v3, v2 quad_perm:[1,0,3,2] row_mask:0xf bank_mask:0xf
	s_and_saveexec_b64 s[2:3], s[0:1]
	s_cbranch_execz .LBB0_2193
	s_waitcnt lgkmcnt(0)
	v_cvt_pk_bf16_f32 v4, v2, v3
	v_add_co_u32_e32 v2, vcc, 0x1a000, v70
	s_nop 1
	v_addc_co_u32_e32 v3, vcc, 0, v71, vcc
	global_store_dword v[2:3], v4, off offset:128
.LBB0_2193:
	s_or_b64 exec, exec, s[2:3]
	v_mul_f32_e32 v1, v16, v1
	s_nop 1
	v_mov_b32_dpp v2, v1 quad_perm:[1,0,3,2] row_mask:0xf bank_mask:0xf
	s_and_saveexec_b64 s[2:3], s[0:1]
	s_cbranch_execz .LBB0_2195
	s_waitcnt lgkmcnt(0)
	v_cvt_pk_bf16_f32 v1, v1, v2
	v_add_co_u32_e32 v2, vcc, 0x1a000, v70
	s_nop 1
	v_addc_co_u32_e32 v3, vcc, 0, v71, vcc
	global_store_dword v[2:3], v1, off offset:192
.LBB0_2195:
	s_or_b64 exec, exec, s[2:3]
	v_rcp_f32_e32 v1, v5
	s_waitcnt lgkmcnt(0)
	v_mul_f32_e32 v2, v65, v1
	s_nop 1
	v_mov_b32_dpp v3, v2 quad_perm:[1,0,3,2] row_mask:0xf bank_mask:0xf
	s_and_saveexec_b64 s[2:3], s[0:1]
	s_cbranch_execz .LBB0_2197
	s_waitcnt lgkmcnt(0)
	v_cvt_pk_bf16_f32 v4, v2, v3
	v_add_co_u32_e32 v2, vcc, 0x1b000, v70
	s_nop 1
	v_addc_co_u32_e32 v3, vcc, 0, v71, vcc
	global_store_dword v[2:3], v4, off
.LBB0_2197:
	s_or_b64 exec, exec, s[2:3]
	v_mul_f32_e32 v2, v49, v1
	s_waitcnt lgkmcnt(0)
	s_nop 1
	v_mov_b32_dpp v3, v2 quad_perm:[1,0,3,2] row_mask:0xf bank_mask:0xf
	s_and_saveexec_b64 s[2:3], s[0:1]
	s_cbranch_execz .LBB0_2199
	s_waitcnt lgkmcnt(0)
	v_cvt_pk_bf16_f32 v4, v2, v3
	v_add_co_u32_e32 v2, vcc, 0x1b000, v70
	s_nop 1
	v_addc_co_u32_e32 v3, vcc, 0, v71, vcc
	global_store_dword v[2:3], v4, off offset:64
.LBB0_2199:
	s_or_b64 exec, exec, s[2:3]
	v_mul_f32_e32 v2, v33, v1
	s_waitcnt lgkmcnt(0)
	s_nop 1
	v_mov_b32_dpp v3, v2 quad_perm:[1,0,3,2] row_mask:0xf bank_mask:0xf
	s_and_saveexec_b64 s[2:3], s[0:1]
	s_cbranch_execz .LBB0_2201
	s_waitcnt lgkmcnt(0)
	v_cvt_pk_bf16_f32 v4, v2, v3
	v_add_co_u32_e32 v2, vcc, 0x1b000, v70
	s_nop 1
	v_addc_co_u32_e32 v3, vcc, 0, v71, vcc
	global_store_dword v[2:3], v4, off offset:128
.LBB0_2201:
	s_or_b64 exec, exec, s[2:3]
	v_mul_f32_e32 v1, v17, v1
	s_nop 1
	v_mov_b32_dpp v2, v1 quad_perm:[1,0,3,2] row_mask:0xf bank_mask:0xf
	s_and_saveexec_b64 s[2:3], s[0:1]
	s_cbranch_execz .LBB0_1874
	s_waitcnt lgkmcnt(0)
	v_cvt_pk_bf16_f32 v1, v1, v2
	v_add_co_u32_e32 v2, vcc, 0x1b000, v70
	s_nop 1
	v_addc_co_u32_e32 v3, vcc, 0, v71, vcc
	global_store_dword v[2:3], v1, off offset:192
	s_branch .LBB0_1874
